# nt hint also on the residual-stream row loads of N1, FIN and N2 (read once per phase)
# speedup vs baseline: 1.0201x; 1.0033x over previous
; #define GAS __attribute__((address_space(1)))
; __device__ __forceinline__ bf16_t* x_row_ptr(Frame& F, int row) { return (bf16_t*)(F.ws + WS_X) + (size_t)row * D; }
; #define N1_ISSUE(R, kk) do { const int kn_ = (kk) < RPW ? (kk) : RPW - 1; rowrq_issue(F, R, rbeg + kn_, F.lane < 16 ? (unsigned)strip[kn_ * 16 + F.lane] : 0xFFFFu); } while (0)
; __device__ __forceinline__ void rowrq_issue(Frame& F, RowRq& R, int row, unsigned ts) {
;     R.row = row; R.ts = ts;
;     const GAS u32x4* xr = (const GAS u32x4*)x_row_ptr(F, row) + 2 * F.lane;
;     R.x[0] = xr[0]; R.x[1] = xr[1];
;     unsigned long long mask = __ballot(ts != 0xFFFFu);
;     unsigned vm = 0u;
; #pragma unroll
;     for (int k = 0; k < 8; ++k) {
;         const bool has = mask != 0ull;
;         const int e = has ? __builtin_ctzll(mask) : 0;
;         const unsigned sl = (unsigned)__builtin_amdgcn_readlane((int)ts, e);
;         mask &= mask - 1ull;
;         R.w[k] = *y_row_ptr16(F, row, has ? e : 0, has ? sl : 0u);
;         vm |= has ? (1u << k) : 0u;
;     }
;     R.vm = vm; R.rest = mask;
; }
; __device__ __forceinline__ void n1_phase(const Frame& F0, int L, int nrows) {
;     ...
;         tokslot_preload(F, strip, rbeg, RPW);
;     ...
;         RowRq R0, R1, R2;
;         N1_ISSUE(R0, 0); N1_ISSUE(R1, 1);
.LBB0_205:
	s_or_b64 exec, exec, s[0:1]
	s_waitcnt lgkmcnt(0)
	s_add_i32 s0, s4, -1
	v_writelane_b32 v255, s0, 25
	s_min_i32 s2, s0, 0
	v_mov_b32_e32 v176, 0xffff
	v_mov_b32_e32 v177, 0xffff
	s_and_saveexec_b64 s[0:1], s[36:37]
	s_lshl_b32 s3, s2, 5
	s_add_i32 s3, s17, s3
	v_lshl_add_u32 v2, v1, 1, s3
	ds_read_u16 v177, v2
	s_or_b64 exec, exec, s[0:1]
	s_add_i32 s44, s38, s2
	s_add_i32 s0, s44, 0xffff8000
	s_lshr_b32 s0, s0, 11
	s_waitcnt lgkmcnt(0)
	v_cmp_ne_u32_e32 vcc, v177, v176
	s_add_i32 s12, s0, 0x100
	s_ashr_i32 s33, s44, 11
	s_add_u32 s0, vcc_lo, -1
	s_addc_u32 s1, vcc_hi, -1
	s_and_b64 s[30:31], s[0:1], vcc
	s_add_u32 s0, s30, -1
	s_addc_u32 s1, s31, -1
	s_and_b64 s[28:29], s[0:1], s[30:31]
	s_add_u32 s0, s28, -1
	s_addc_u32 s1, s29, -1
	s_and_b64 s[22:23], s[0:1], s[28:29]
	s_add_u32 s0, s22, -1
	s_addc_u32 s1, s23, -1
	s_and_b64 s[10:11], s[0:1], s[22:23]
	s_add_u32 s0, s10, -1
	s_addc_u32 s1, s11, -1
	s_and_b64 s[8:9], s[0:1], s[10:11]
	s_add_u32 s0, s8, -1
	s_addc_u32 s1, s9, -1
	s_and_b64 s[0:1], s[0:1], s[8:9]
	s_cmp_eq_u64 s[0:1], 0
	s_cselect_b64 s[4:5], -1, 0
	s_ff1_i32_b64 s6, s[0:1]
	s_and_b64 s[2:3], s[4:5], exec
	s_cselect_b32 s19, 0, s6
	s_add_u32 s2, s0, -1
	s_addc_u32 s3, s1, -1
	s_and_b64 s[0:1], s[2:3], s[0:1]
	s_lshl_b32 s2, s19, 4
	s_add_i32 s18, s2, s33
	s_lshl_b32 s35, s19, 1
	s_cmp_eq_u64 s[0:1], 0
	s_cselect_b64 s[2:3], -1, 0
	s_ff1_i32_b64 s25, s[0:1]
	s_and_b64 s[6:7], s[2:3], exec
	s_cselect_b32 s25, 0, s25
	s_lshl_b32 s6, s25, 4
	s_lshl_b32 s7, s25, 1
	s_add_i32 s6, s6, s33
	s_add_i32 s7, s7, s12
	s_cmp_lt_i32 s44, 0x8000
	s_cselect_b32 s34, s6, s7
	s_add_i32 s35, s35, s12
	s_cmp_lt_i32 s44, 0x8000
	s_cselect_b32 s18, s18, s35
	s_cmp_eq_u64 s[8:9], 0
	s_cselect_b64 s[6:7], -1, 0
	s_ff1_i32_b64 s35, s[8:9]
	s_and_b64 s[8:9], s[6:7], exec
	s_cselect_b32 s35, 0, s35
	s_lshl_b32 s8, s35, 4
	s_lshl_b32 s9, s35, 1
	s_add_i32 s8, s8, s33
	s_add_i32 s9, s9, s12
	s_cmp_lt_i32 s44, 0x8000
	s_cselect_b32 s40, s8, s9
	s_cmp_eq_u64 s[10:11], 0
	s_cselect_b64 s[8:9], -1, 0
	s_ff1_i32_b64 s39, s[10:11]
	s_and_b64 s[10:11], s[8:9], exec
	s_cselect_b32 s39, 0, s39
	s_lshl_b32 s10, s39, 4
	s_lshl_b32 s11, s39, 1
	s_add_i32 s10, s10, s33
	s_add_i32 s11, s11, s12
	s_cmp_lt_i32 s44, 0x8000
	s_cselect_b32 s42, s10, s11
	s_cmp_eq_u64 s[22:23], 0
	s_cselect_b64 s[10:11], -1, 0
	s_ff1_i32_b64 s41, s[22:23]
	s_and_b64 s[22:23], s[10:11], exec
	s_cselect_b32 s41, 0, s41
	s_lshl_b32 s22, s41, 4
	s_lshl_b32 s23, s41, 1
	s_add_i32 s22, s22, s33
	s_add_i32 s23, s23, s12
	s_cmp_lt_i32 s44, 0x8000
	s_cselect_b32 s46, s22, s23
	s_cmp_eq_u64 s[28:29], 0
	s_cselect_b64 s[22:23], -1, 0
	s_ff1_i32_b64 s43, s[28:29]
	s_and_b64 s[28:29], s[22:23], exec
	s_cselect_b32 s43, 0, s43
	s_lshl_b32 s28, s43, 4
	s_lshl_b32 s29, s43, 1
	s_add_i32 s28, s28, s33
	s_add_i32 s29, s29, s12
	s_cmp_lt_i32 s44, 0x8000
	s_cselect_b32 s48, s28, s29
	s_cmp_eq_u64 s[30:31], 0
	s_cselect_b64 s[28:29], -1, 0
	s_ff1_i32_b64 s45, s[30:31]
	s_and_b64 s[30:31], s[28:29], exec
	s_cselect_b32 s47, 0, s45
	s_lshl_b32 s30, s47, 4
	s_lshl_b32 s31, s47, 1
	s_add_i32 s30, s30, s33
	s_add_i32 s31, s31, s12
	s_cmp_lt_i32 s44, 0x8000
	s_cselect_b32 s50, s30, s31
	s_cmp_lg_u64 vcc, 0
	s_cselect_b64 s[30:31], -1, 0
	s_ff1_i32_b64 s45, vcc
	s_and_b64 s[52:53], s[30:31], exec
	s_cselect_b32 s49, s45, 0
	s_lshl_b32 s45, s49, 4
	s_add_i32 s45, s45, s33
	s_lshl_b32 s33, s49, 1
	s_add_i32 s33, s33, s12
	s_cmp_lt_i32 s44, 0x8000
	s_cselect_b32 s52, s45, s33
	s_ashr_i32 s45, s44, 31
	s_lshl_b64 s[54:55], s[44:45], 11
	v_readlane_b32 s56, v252, 20
	v_readlane_b32 s57, v252, 21
	s_add_u32 s54, s56, s54
	s_addc_u32 s55, s57, s55
	v_lshlrev_b32_e32 v2, 5, v1
	v_readlane_b32 s12, v177, s49
	s_ashr_i32 s53, s52, 31
	global_load_dwordx4 v[106:109], v2, s[54:55] offset:16 nt
	global_load_dwordx4 v[110:113], v2, s[54:55] nt
	s_lshl_b64 s[52:53], s[52:53], 18
	s_lshl_b64 s[54:55], s[12:13], 10
	s_and_b64 s[56:57], s[30:31], exec
	s_cselect_b32 s12, s55, 0
	s_cselect_b32 s33, s54, 0
	s_add_u32 s45, s90, s52
	s_addc_u32 s49, s91, s53
	s_add_u32 s52, s45, s33
	s_addc_u32 s53, s49, s12
	v_readlane_b32 s12, v177, s47
	s_ashr_i32 s51, s50, 31
	s_lshl_b64 s[50:51], s[50:51], 18
	s_lshl_b64 s[54:55], s[12:13], 10
	s_and_b64 s[56:57], s[28:29], exec
	s_cselect_b32 s12, 0, s55
	s_cselect_b32 s33, 0, s54
	s_add_u32 s45, s90, s50
	s_addc_u32 s47, s91, s51
	s_add_u32 s50, s45, s33
	v_lshlrev_b32_e32 v154, 4, v1
	s_addc_u32 s51, s47, s12
	v_readlane_b32 s12, v177, s43
	s_ashr_i32 s49, s48, 31
	global_load_dwordx4 v[102:105], v154, s[52:53]
	global_load_dwordx4 v[98:101], v154, s[50:51]
	s_lshl_b64 s[48:49], s[48:49], 18
	s_lshl_b64 s[50:51], s[12:13], 10
	s_and_b64 s[52:53], s[22:23], exec
	s_cselect_b32 s12, 0, s51
	s_cselect_b32 s33, 0, s50
	s_add_u32 s43, s90, s48
	s_addc_u32 s45, s91, s49
	s_add_u32 s48, s43, s33
	s_addc_u32 s49, s45, s12
	v_readlane_b32 s12, v177, s41
	s_ashr_i32 s47, s46, 31
	s_lshl_b64 s[46:47], s[46:47], 18
	s_lshl_b64 s[50:51], s[12:13], 10
	s_and_b64 s[52:53], s[10:11], exec
	s_cselect_b32 s12, 0, s51
	s_cselect_b32 s33, 0, s50
	s_add_u32 s41, s90, s46
	s_addc_u32 s43, s91, s47
	s_add_u32 s46, s41, s33
	s_addc_u32 s47, s43, s12
	v_readlane_b32 s12, v177, s39
	s_ashr_i32 s43, s42, 31
	global_load_dwordx4 v[94:97], v154, s[48:49]
	global_load_dwordx4 v[90:93], v154, s[46:47]
	s_lshl_b64 s[42:43], s[42:43], 18
	s_lshl_b64 s[46:47], s[12:13], 10
	s_and_b64 s[48:49], s[8:9], exec
	s_cselect_b32 s12, 0, s47
	s_cselect_b32 s33, 0, s46
	s_add_u32 s39, s90, s42
	s_addc_u32 s41, s91, s43
	s_add_u32 s42, s39, s33
	s_addc_u32 s43, s41, s12
	v_readlane_b32 s12, v177, s35
	s_ashr_i32 s41, s40, 31
	s_lshl_b64 s[40:41], s[40:41], 18
	s_lshl_b64 s[46:47], s[12:13], 10
	s_and_b64 s[48:49], s[6:7], exec
	s_cselect_b32 s12, 0, s47
	s_cselect_b32 s33, 0, s46
	s_add_u32 s35, s90, s40
	s_addc_u32 s39, s91, s41
	s_add_u32 s40, s35, s33
	s_addc_u32 s41, s39, s12
	v_readlane_b32 s12, v177, s19
	s_ashr_i32 s19, s18, 31
	global_load_dwordx4 v[86:89], v154, s[42:43]
	global_load_dwordx4 v[82:85], v154, s[40:41]
	s_lshl_b64 s[18:19], s[18:19], 18
	s_lshl_b64 s[40:41], s[12:13], 10
	s_and_b64 s[42:43], s[4:5], exec
	s_cselect_b32 s12, 0, s41
	s_cselect_b32 s33, 0, s40
	s_add_u32 s18, s90, s18
	s_addc_u32 s19, s91, s19
	s_add_u32 s18, s18, s33
	s_addc_u32 s19, s19, s12
	v_readlane_b32 s12, v177, s25
	s_ashr_i32 s35, s34, 31
	s_lshl_b64 s[34:35], s[34:35], 18
	s_lshl_b64 s[40:41], s[12:13], 10
	s_and_b64 s[42:43], s[2:3], exec
	s_cselect_b32 s12, 0, s41
	s_cselect_b32 s25, 0, s40
	s_add_u32 s33, s90, s34
	s_addc_u32 s35, s91, s35
	s_add_u32 s34, s33, s25
	s_addc_u32 s35, s35, s12
	global_load_dwordx4 v[78:81], v154, s[18:19]
	global_load_dwordx4 v[62:65], v154, s[34:35]
	v_readlane_b32 s12, v255, 25
	s_min_i32 s12, s12, 1
	s_and_saveexec_b64 s[18:19], s[36:37]
	s_lshl_b32 s25, s12, 5
	s_add_i32 s25, s17, s25
	v_lshl_add_u32 v2, v1, 1, s25
	ds_read_u16 v176, v2
	s_or_b64 exec, exec, s[18:19]
	s_add_i32 s40, s38, s12
	s_mov_b32 s12, 0xffff
	s_waitcnt lgkmcnt(0)
; #define GAS __attribute__((address_space(1)))
; __device__ __forceinline__ bf16_t* x_row_ptr(Frame& F, int row) { return (bf16_t*)(F.ws + WS_X) + (size_t)row * D; }
; __device__ __forceinline__ void rowrq_issue(Frame& F, RowRq& R, int row, unsigned ts) {
;     R.row = row; R.ts = ts;
;     const GAS u32x4* xr = (const GAS u32x4*)x_row_ptr(F, row) + 2 * F.lane;
;     R.x[0] = xr[0]; R.x[1] = xr[1];
;     unsigned long long mask = __ballot(ts != 0xFFFFu);
;     unsigned vm = 0u;
; #pragma unroll
;     for (int k = 0; k < 8; ++k) {
;         const bool has = mask != 0ull;
;         const int e = has ? __builtin_ctzll(mask) : 0;
;         const unsigned sl = (unsigned)__builtin_amdgcn_readlane((int)ts, e);
;         mask &= mask - 1ull;
;         R.w[k] = *y_row_ptr16(F, row, has ? e : 0, has ? sl : 0u);
;         vm |= has ? (1u << k) : 0u;
;     }
;     R.vm = vm; R.rest = mask;
; }
	v_cmp_ne_u32_e32 vcc, s12, v176
	s_add_i32 s12, s40, 0xffff8000
	s_lshr_b32 s12, s12, 11
	s_addk_i32 s12, 0x100
	s_ashr_i32 s41, s40, 11
	s_add_u32 s18, vcc_lo, -1
	s_addc_u32 s19, vcc_hi, -1
	s_and_b64 s[18:19], s[18:19], vcc
	s_add_u32 s34, s18, -1
	s_addc_u32 s35, s19, -1
	s_and_b64 s[62:63], s[34:35], s[18:19]
	s_add_u32 s34, s62, -1
	s_addc_u32 s35, s63, -1
	s_and_b64 s[46:47], s[34:35], s[62:63]
	s_add_u32 s34, s46, -1
	s_addc_u32 s35, s47, -1
	s_and_b64 s[58:59], s[34:35], s[46:47]
	s_add_u32 s34, s58, -1
	s_addc_u32 s35, s59, -1
	s_and_b64 s[54:55], s[34:35], s[58:59]
	s_add_u32 s34, s54, -1
	s_addc_u32 s35, s55, -1
	s_and_b64 s[34:35], s[34:35], s[54:55]
	s_cmp_eq_u64 s[34:35], 0
	s_cselect_b64 s[50:51], -1, 0
	s_ff1_i32_b64 s25, s[34:35]
	s_and_b64 s[42:43], s[50:51], exec
	s_cselect_b32 s25, 0, s25
	s_add_u32 s42, s34, -1
	s_addc_u32 s43, s35, -1
	s_lshl_b32 s33, s25, 4
	s_and_b64 s[42:43], s[42:43], s[34:35]
	s_add_i32 s39, s33, s41
	s_lshl_b32 s45, s25, 1
	s_cmp_eq_u64 s[42:43], 0
	s_cselect_b64 s[34:35], -1, 0
	s_ff1_i32_b64 s33, s[42:43]
	s_and_b64 s[48:49], s[34:35], exec
	s_cselect_b32 s33, 0, s33
	s_lshl_b32 s48, s33, 4
	s_lshl_b32 s49, s33, 1
	s_add_i32 s48, s48, s41
	s_add_i32 s49, s49, s12
	s_cmp_lt_i32 s40, 0x8000
	s_cselect_b32 s48, s48, s49
	s_add_i32 s45, s45, s12
	s_cmp_lt_i32 s40, 0x8000
	s_cselect_b32 s56, s39, s45
	s_cmp_eq_u64 s[54:55], 0
	s_cselect_b64 s[52:53], -1, 0
	s_ff1_i32_b64 s39, s[54:55]
	s_and_b64 s[54:55], s[52:53], exec
	s_cselect_b32 s39, 0, s39
	s_lshl_b32 s45, s39, 4
	s_lshl_b32 s49, s39, 1
	s_add_i32 s45, s45, s41
	s_add_i32 s49, s49, s12
	s_cmp_lt_i32 s40, 0x8000
	s_cselect_b32 s64, s45, s49
	s_cmp_eq_u64 s[58:59], 0
	s_cselect_b64 s[54:55], -1, 0
	s_ff1_i32_b64 s45, s[58:59]
	s_and_b64 s[58:59], s[54:55], exec
	s_cselect_b32 s45, 0, s45
	s_lshl_b32 s49, s45, 4
	s_lshl_b32 s57, s45, 1
	s_add_i32 s49, s49, s41
	s_add_i32 s57, s57, s12
	s_cmp_lt_i32 s40, 0x8000
	s_cselect_b32 s66, s49, s57
	s_cmp_eq_u64 s[46:47], 0
	s_cselect_b64 s[58:59], -1, 0
	s_ff1_i32_b64 s49, s[46:47]
	s_and_b64 s[46:47], s[58:59], exec
	s_cselect_b32 s46, 0, s49
	s_lshl_b32 s47, s46, 4
	s_lshl_b32 s49, s46, 1
	s_add_i32 s47, s47, s41
	s_add_i32 s49, s49, s12
	s_cmp_lt_i32 s40, 0x8000
	s_cselect_b32 s68, s47, s49
	s_cmp_eq_u64 s[62:63], 0
	s_cselect_b64 s[60:61], -1, 0
	s_ff1_i32_b64 s47, s[62:63]
	s_and_b64 s[62:63], s[60:61], exec
	s_cselect_b32 s47, 0, s47
	s_lshl_b32 s49, s47, 4
	s_lshl_b32 s57, s47, 1
	s_add_i32 s49, s49, s41
	s_add_i32 s57, s57, s12
	s_cmp_lt_i32 s40, 0x8000
	s_cselect_b32 s70, s49, s57
	s_cmp_eq_u64 s[18:19], 0
	s_cselect_b64 s[62:63], -1, 0
	s_ff1_i32_b64 s49, s[18:19]
	s_and_b64 s[18:19], s[62:63], exec
	s_cselect_b32 s18, 0, s49
	s_lshl_b32 s19, s18, 4
	s_lshl_b32 s49, s18, 1
	s_add_i32 s19, s19, s41
	s_add_i32 s49, s49, s12
	s_cmp_lt_i32 s40, 0x8000
	s_cselect_b32 s72, s19, s49
	s_cmp_lg_u64 vcc, 0
	s_cselect_b64 s[74:75], -1, 0
	s_ff1_i32_b64 s19, vcc
	s_and_b64 s[76:77], s[74:75], exec
	s_cselect_b32 s19, s19, 0
	s_lshl_b32 s49, s19, 4
	s_add_i32 s49, s49, s41
	s_lshl_b32 s41, s19, 1
	s_add_i32 s41, s41, s12
	s_cmp_lt_i32 s40, 0x8000
	s_cselect_b32 s76, s49, s41
	s_add_u32 s78, s0, -1
	s_addc_u32 s79, s1, -1
	s_and_b64 s[0:1], s[78:79], s[0:1]
	s_and_b64 s[4:5], s[4:5], exec
	s_cselect_b32 s12, 0, 64
	s_and_b64 s[4:5], s[6:7], exec
	s_cselect_b32 s6, 0, 32
	s_and_b64 s[4:5], s[8:9], exec
	s_cselect_b32 s7, 0, 16
	s_and_b64 s[4:5], s[10:11], exec
	s_cselect_b32 s8, 0, 8
	s_and_b64 s[4:5], s[22:23], exec
	v_cndmask_b32_e64 v4, 0, 1, s[30:31]
	s_cselect_b32 s9, 0, 4
	s_and_b64 s[4:5], s[28:29], exec
	s_cselect_b32 s4, 0, 2
	v_readfirstlane_b32 s5, v4
	s_or_b32 s4, s4, s5
	s_or_b32 s4, s4, s9
	s_or_b32 s4, s4, s8
	s_or_b32 s4, s4, s7
	s_or_b32 s4, s4, s6
	s_or_b32 s4, s4, s12
	s_and_b64 s[2:3], s[2:3], exec
	s_cselect_b32 s2, 0, 0x80
	s_ashr_i32 s41, s40, 31
	s_or_b32 s5, s4, s2
	s_lshl_b64 s[2:3], s[40:41], 11
	v_readlane_b32 s22, v252, 20
	v_lshlrev_b32_e32 v2, 1, v1
	v_readlane_b32 s23, v252, 21
	s_add_u32 s2, s22, s2
	s_addc_u32 s3, s23, s3
	v_lshlrev_b32_e32 v156, 4, v2
	v_readlane_b32 s12, v176, s19
	s_ashr_i32 s77, s76, 31
; #define GAS __attribute__((address_space(1)))
; __device__ __forceinline__ bf16_t* x_row_ptr(Frame& F, int row) { return (bf16_t*)(F.ws + WS_X) + (size_t)row * D; }
; #define N1_ISSUE(R, kk) do { const int kn_ = (kk) < RPW ? (kk) : RPW - 1; rowrq_issue(F, R, rbeg + kn_, F.lane < 16 ? (unsigned)strip[kn_ * 16 + F.lane] : 0xFFFFu); } while (0)
; #define N1_STEP(RC, RI, kk) do { const int k_ = (kk), row_ = rbeg + k_; N1_MOD16(row_); N1_ISSUE(RI, k_ + 2); f32x4 v_[4]; rowrq_consume(F, RC, v_); n1_finish16(F, L, row_, v_, gs, sh); } while (0)
; __device__ __forceinline__ void rowrq_issue(Frame& F, RowRq& R, int row, unsigned ts) {
;     R.row = row; R.ts = ts;
;     const GAS u32x4* xr = (const GAS u32x4*)x_row_ptr(F, row) + 2 * F.lane;
;     R.x[0] = xr[0]; R.x[1] = xr[1];
;     unsigned long long mask = __ballot(ts != 0xFFFFu);
;     unsigned vm = 0u;
; #pragma unroll
;     for (int k = 0; k < 8; ++k) {
;         const bool has = mask != 0ull;
;         const int e = has ? __builtin_ctzll(mask) : 0;
;         const unsigned sl = (unsigned)__builtin_amdgcn_readlane((int)ts, e);
;         mask &= mask - 1ull;
;         R.w[k] = *y_row_ptr16(F, row, has ? e : 0, has ? sl : 0u);
;         vm |= has ? (1u << k) : 0u;
;     }
;     R.vm = vm; R.rest = mask;
; }
; __device__ __forceinline__ void n1_phase(const Frame& F0, int L, int nrows) {
;     ...
;         N1_ISSUE(R0, 0); N1_ISSUE(R1, 1);
;         int k = 0;
;         for (; k + 2 < RPW; k += 3) { N1_STEP(R0, R2, k); N1_STEP(R1, R0, k + 1); N1_STEP(R2, R1, k + 2); }
	global_load_dwordx4 v[70:73], v156, s[2:3] offset:16 nt
	global_load_dwordx4 v[74:77], v156, s[2:3] nt
	s_lshl_b64 s[2:3], s[76:77], 18
	s_lshl_b64 s[6:7], s[12:13], 10
	s_and_b64 s[8:9], s[74:75], exec
	s_cselect_b32 s4, s7, 0
	s_cselect_b32 s6, s6, 0
	s_add_u32 s2, s90, s2
	s_addc_u32 s3, s91, s3
	s_add_u32 s2, s2, s6
	s_addc_u32 s3, s3, s4
	v_readlane_b32 s12, v176, s18
	s_ashr_i32 s73, s72, 31
	s_lshl_b64 s[6:7], s[72:73], 18
	s_lshl_b64 s[8:9], s[12:13], 10
	s_and_b64 s[10:11], s[62:63], exec
	s_cselect_b32 s4, 0, s9
	s_cselect_b32 s8, 0, s8
	s_add_u32 s6, s90, s6
	s_addc_u32 s7, s91, s7
	s_add_u32 s6, s6, s8
	s_addc_u32 s7, s7, s4
	v_readlane_b32 s12, v176, s47
	s_ashr_i32 s71, s70, 31
	global_load_dwordx4 v[66:69], v154, s[2:3]
	global_load_dwordx4 v[58:61], v154, s[6:7]
	s_lshl_b64 s[2:3], s[70:71], 18
	s_lshl_b64 s[6:7], s[12:13], 10
	s_and_b64 s[8:9], s[60:61], exec
	s_cselect_b32 s4, 0, s7
	s_cselect_b32 s6, 0, s6
	s_add_u32 s2, s90, s2
	s_addc_u32 s3, s91, s3
	s_add_u32 s2, s2, s6
	s_addc_u32 s3, s3, s4
	v_readlane_b32 s12, v176, s46
	s_ashr_i32 s69, s68, 31
	s_lshl_b64 s[6:7], s[68:69], 18
	s_lshl_b64 s[8:9], s[12:13], 10
	s_and_b64 s[10:11], s[58:59], exec
	s_cselect_b32 s4, 0, s9
	s_cselect_b32 s8, 0, s8
	s_add_u32 s6, s90, s6
	s_addc_u32 s7, s91, s7
	s_add_u32 s6, s6, s8
	s_addc_u32 s7, s7, s4
	v_readlane_b32 s12, v176, s45
	s_ashr_i32 s67, s66, 31
	global_load_dwordx4 v[54:57], v154, s[2:3]
	global_load_dwordx4 v[50:53], v154, s[6:7]
	s_lshl_b64 s[2:3], s[66:67], 18
	s_lshl_b64 s[6:7], s[12:13], 10
	s_and_b64 s[8:9], s[54:55], exec
	s_cselect_b32 s4, 0, s7
	s_cselect_b32 s6, 0, s6
	s_add_u32 s2, s90, s2
	s_addc_u32 s3, s91, s3
	s_add_u32 s2, s2, s6
	s_addc_u32 s3, s3, s4
	v_readlane_b32 s12, v176, s39
	s_ashr_i32 s65, s64, 31
	s_lshl_b64 s[6:7], s[64:65], 18
	s_lshl_b64 s[8:9], s[12:13], 10
	s_and_b64 s[10:11], s[52:53], exec
	s_cselect_b32 s4, 0, s9
	s_cselect_b32 s8, 0, s8
	s_add_u32 s6, s90, s6
	s_addc_u32 s7, s91, s7
	s_add_u32 s6, s6, s8
	s_addc_u32 s7, s7, s4
	v_readlane_b32 s12, v176, s25
	s_ashr_i32 s57, s56, 31
	global_load_dwordx4 v[46:49], v154, s[2:3]
	global_load_dwordx4 v[42:45], v154, s[6:7]
	s_lshl_b64 s[2:3], s[56:57], 18
	s_lshl_b64 s[6:7], s[12:13], 10
	s_and_b64 s[8:9], s[50:51], exec
	s_cselect_b32 s4, 0, s7
	s_cselect_b32 s6, 0, s6
	s_add_u32 s2, s90, s2
	s_addc_u32 s3, s91, s3
	s_add_u32 s2, s2, s6
	s_addc_u32 s3, s3, s4
	s_add_u32 s6, s42, -1
	s_addc_u32 s7, s43, -1
	s_and_b64 s[42:43], s[6:7], s[42:43]
	s_and_b64 s[6:7], s[50:51], exec
	s_cselect_b32 s4, 0, 64
	s_and_b64 s[6:7], s[52:53], exec
	s_cselect_b32 s8, 0, 32
	s_and_b64 s[6:7], s[54:55], exec
	s_cselect_b32 s9, 0, 16
	s_and_b64 s[6:7], s[58:59], exec
	s_cselect_b32 s10, 0, 8
	s_and_b64 s[6:7], s[60:61], exec
	v_cndmask_b32_e64 v3, 0, 1, s[74:75]
	s_cselect_b32 s11, 0, 4
	s_and_b64 s[6:7], s[62:63], exec
	s_cselect_b32 s6, 0, 2
	v_readfirstlane_b32 s7, v3
	s_or_b32 s6, s6, s7
	s_or_b32 s6, s6, s11
	s_or_b32 s6, s6, s10
	s_or_b32 s6, s6, s9
	v_readlane_b32 s12, v176, s33
	s_or_b32 s6, s6, s8
	s_ashr_i32 s49, s48, 31
	s_or_b32 s4, s6, s4
	s_lshl_b64 s[6:7], s[48:49], 18
	s_lshl_b64 s[8:9], s[12:13], 10
	s_and_b64 s[10:11], s[34:35], exec
	s_cselect_b32 s9, 0, s9
	s_cselect_b32 s8, 0, s8
	s_add_u32 s6, s90, s6
	s_addc_u32 s7, s91, s7
	s_add_u32 s6, s6, s8
	s_addc_u32 s7, s7, s9
	global_load_dwordx4 v[38:41], v154, s[2:3]
	global_load_dwordx4 v[34:37], v154, s[6:7]
	s_and_b64 s[2:3], s[34:35], exec
	s_cselect_b32 s2, 0, 0x80
	s_or_b32 s41, s4, s2
	v_readlane_b32 s3, v255, 22
	s_mov_b32 s25, 0
	s_cmp_lt_i32 s3, 3
	s_mov_b32 s39, -1
	s_cbranch_scc1 .LBB0_310
	v_readlane_b32 s2, v255, 17
	v_readlane_b32 s3, v255, 18
	s_bitcmp1_b32 s2, 0
	v_readlane_b32 s2, v255, 23
	v_mov_b32_e32 v155, v191
	v_lshlrev_b32_e32 v190, 6, v1
	v_readlane_b32 s3, v255, 24
	v_mov_b32_e32 v157, v191
	v_lshl_add_u32 v178, v1, 1, s17
	s_cselect_b64 s[48:49], -1, 0
	v_lshl_add_u64 v[158:159], s[2:3], 0, v[190:191]
	v_lshl_add_u64 v[160:161], s[22:23], 0, v[156:157]
	v_lshl_add_u64 v[162:163], s[96:97], 0, v[156:157]
	v_lshl_add_u64 v[164:165], s[96:97], 0, v[154:155]
	s_mov_b32 s33, 0

; #define GAS __attribute__((address_space(1)))
; __device__ __forceinline__ bf16_t* x_row_ptr(Frame& F, int row) { return (bf16_t*)(F.ws + WS_X) + (size_t)row * D; }
; __device__ __forceinline__ void rowrq_issue(Frame& F, RowRq& R, int row, unsigned ts) {
;     R.row = row; R.ts = ts;
;     const GAS u32x4* xr = (const GAS u32x4*)x_row_ptr(F, row) + 2 * F.lane;
;     R.x[0] = xr[0]; R.x[1] = xr[1];
;     unsigned long long mask = __ballot(ts != 0xFFFFu);
;     unsigned vm = 0u;
; #pragma unroll
;     for (int k = 0; k < 8; ++k) {
;         const bool has = mask != 0ull;
;         const int e = has ? __builtin_ctzll(mask) : 0;
;         const unsigned sl = (unsigned)__builtin_amdgcn_readlane((int)ts, e);
;         mask &= mask - 1ull;
;         R.w[k] = *y_row_ptr16(F, row, has ? e : 0, has ? sl : 0u);
;         vm |= has ? (1u << k) : 0u;
;     }
;     R.vm = vm; R.rest = mask;
; }
.LBB0_213:
	s_add_i32 s6, s33, 2
	v_mov_b32_e32 v155, 0xffff
	s_and_saveexec_b64 s[2:3], s[36:37]
	v_lshl_add_u32 v114, s6, 5, v178
	ds_read_u16 v155, v114
	s_or_b64 exec, exec, s[2:3]
	s_add_i32 s50, s6, s38
	s_mov_b32 s2, 0xffff
	s_waitcnt lgkmcnt(0)
	v_cmp_ne_u32_e32 vcc, s2, v155
	s_add_i32 s2, s50, 0xffff8000
	s_lshr_b32 s17, s2, 11
	s_addk_i32 s17, 0x100
	s_ashr_i32 s66, s50, 11
	s_add_u32 s2, vcc_lo, -1
	s_addc_u32 s3, vcc_hi, -1
	s_and_b64 s[64:65], s[2:3], vcc
	s_add_u32 s2, s64, -1
	s_addc_u32 s3, s65, -1
	s_and_b64 s[60:61], s[2:3], s[64:65]
	s_add_u32 s2, s60, -1
	s_addc_u32 s3, s61, -1
	s_and_b64 s[34:35], s[2:3], s[60:61]
	s_add_u32 s2, s34, -1
	s_addc_u32 s3, s35, -1
	s_and_b64 s[18:19], s[2:3], s[34:35]
	s_add_u32 s2, s18, -1
	s_addc_u32 s3, s19, -1
	s_and_b64 s[22:23], s[2:3], s[18:19]
	s_add_u32 s2, s22, -1
	s_addc_u32 s3, s23, -1
	s_and_b64 s[10:11], s[2:3], s[22:23]
	s_cmp_eq_u64 s[10:11], 0
	s_cselect_b64 s[6:7], -1, 0
	s_ff1_i32_b64 s8, s[10:11]
	s_and_b64 s[2:3], s[6:7], exec
	s_cselect_b32 s25, 0, s8
	s_add_u32 s2, s10, -1
	s_addc_u32 s3, s11, -1
	s_and_b64 s[56:57], s[2:3], s[10:11]
	s_lshl_b32 s2, s25, 4
	s_add_i32 s12, s2, s66
	s_lshl_b32 s30, s25, 1
	s_cmp_eq_u64 s[56:57], 0
	s_cselect_b64 s[2:3], -1, 0
	s_ff1_i32_b64 s28, s[56:57]
	s_and_b64 s[8:9], s[2:3], exec
	s_cselect_b32 s9, 0, s28
	s_lshl_b32 s8, s9, 4
	s_lshl_b32 s28, s9, 1
	s_add_i32 s8, s8, s66
	s_add_i32 s31, s28, s17
	s_cmp_lt_i32 s50, 0x8000
	s_cselect_b64 s[28:29], -1, 0
	s_and_b64 s[28:29], s[28:29], exec
	s_cselect_b32 s8, s8, s31
	s_add_i32 s30, s30, s17
	s_cmp_lt_i32 s50, 0x8000
	s_cselect_b64 s[28:29], -1, 0
	s_and_b64 s[28:29], s[28:29], exec
	s_cselect_b32 s28, s12, s30
	s_cmp_eq_u64 s[22:23], 0
	s_cselect_b64 s[30:31], -1, 0
	s_ff1_i32_b64 s12, s[22:23]
	s_and_b64 s[46:47], s[30:31], exec
	s_cselect_b32 s29, 0, s12
	s_lshl_b32 s12, s29, 4
	s_lshl_b32 s45, s29, 1
	s_add_i32 s12, s12, s66
	s_add_i32 s45, s45, s17
	s_cmp_lt_i32 s50, 0x8000
	s_cselect_b64 s[46:47], -1, 0
	s_and_b64 s[46:47], s[46:47], exec
	s_cselect_b32 s58, s12, s45
	s_cmp_eq_u64 s[18:19], 0
	s_cselect_b64 s[62:63], -1, 0
	s_ff1_i32_b64 s12, s[18:19]
	s_and_b64 s[46:47], s[62:63], exec
	s_cselect_b32 s45, 0, s12
	s_lshl_b32 s12, s45, 4
	s_lshl_b32 s46, s45, 1
	s_add_i32 s12, s12, s66
	s_add_i32 s51, s46, s17
	s_cmp_lt_i32 s50, 0x8000
	s_cselect_b64 s[46:47], -1, 0
	s_and_b64 s[46:47], s[46:47], exec
	s_cselect_b32 s46, s12, s51
	s_cmp_eq_u64 s[34:35], 0
	s_cselect_b64 s[74:75], -1, 0
	s_ff1_i32_b64 s12, s[34:35]
	s_and_b64 s[52:53], s[74:75], exec
	s_cselect_b32 s47, 0, s12
	s_lshl_b32 s12, s47, 4
	s_lshl_b32 s51, s47, 1
	s_add_i32 s12, s12, s66
	s_add_i32 s51, s51, s17
	s_cmp_lt_i32 s50, 0x8000
	s_cselect_b64 s[52:53], -1, 0
	s_and_b64 s[52:53], s[52:53], exec
	s_cselect_b32 s76, s12, s51
	s_cmp_eq_u64 s[60:61], 0
	s_cselect_b64 s[78:79], -1, 0
	s_ff1_i32_b64 s12, s[60:61]
	s_and_b64 s[52:53], s[78:79], exec
	s_cselect_b32 s59, 0, s12
	s_lshl_b32 s12, s59, 4
	s_lshl_b32 s51, s59, 1
	s_add_i32 s12, s12, s66
	s_add_i32 s51, s51, s17
	s_cmp_lt_i32 s50, 0x8000
	s_cselect_b64 s[52:53], -1, 0
	s_and_b64 s[52:53], s[52:53], exec
	s_cselect_b32 s84, s12, s51
	s_cmp_eq_u64 s[64:65], 0
	s_cselect_b64 s[68:69], -1, 0
	s_ff1_i32_b64 s12, s[64:65]
	s_and_b64 s[52:53], s[68:69], exec
	s_cselect_b32 s67, 0, s12
	s_lshl_b32 s12, s67, 4
	s_lshl_b32 s51, s67, 1
	s_add_i32 s12, s12, s66
	s_add_i32 s51, s51, s17
	s_cmp_lt_i32 s50, 0x8000
	s_cselect_b64 s[52:53], -1, 0
	s_and_b64 s[52:53], s[52:53], exec
	s_cselect_b32 s86, s12, s51
	s_cmp_eq_u64 vcc, 0
	s_cselect_b64 s[70:71], -1, 0
	s_ff1_i32_b64 s12, vcc
	s_and_b64 s[52:53], s[70:71], exec
	s_cselect_b32 s12, 0, s12
	s_lshl_b32 s51, s12, 4
	s_lshl_b32 s52, s12, 1
	s_add_i32 s51, s51, s66
	s_add_i32 s72, s52, s17
	s_cmp_lt_i32 s50, 0x8000
	s_cselect_b64 s[54:55], -1, 0
	s_and_b64 s[52:53], s[54:55], exec
	s_cselect_b32 s88, s51, s72
	s_ashr_i32 s51, s50, 31
	s_lshl_b64 s[52:53], s[50:51], 11
	s_cmp_lg_u64 vcc, 0
	s_cselect_b64 s[72:73], -1, 0
	v_readlane_b32 s12, v155, s12
	s_ashr_i32 s89, s88, 31
	s_lshl_b64 s[88:89], s[88:89], 18
	s_lshl_b64 s[92:93], s[12:13], 10
	v_writelane_b32 v255, s52, 26
	s_and_b64 s[70:71], s[70:71], exec
	s_cselect_b32 s12, 0, s93
	v_writelane_b32 v255, s53, 27
	v_lshl_add_u64 v[166:167], v[160:161], 0, s[52:53]
	s_cselect_b32 s52, 0, s92
	s_add_u32 s53, s90, s88
	s_addc_u32 s70, s91, s89
	s_add_u32 s88, s53, s52
	s_addc_u32 s89, s70, s12
	s_cmp_lg_u64 s[64:65], 0
	s_cselect_b64 s[70:71], -1, 0
	v_readlane_b32 s12, v155, s67
	s_ashr_i32 s87, s86, 31
	s_lshl_b64 s[64:65], s[86:87], 18
	s_lshl_b64 s[86:87], s[12:13], 10
	s_and_b64 s[68:69], s[68:69], exec
	s_cselect_b32 s12, 0, s87
	s_cselect_b32 s52, 0, s86
	s_add_u32 s53, s90, s64
	s_addc_u32 s65, s91, s65
	s_add_u32 s64, s53, s52
	s_addc_u32 s65, s65, s12
	s_cmp_lg_u64 s[60:61], 0
	s_cselect_b64 s[52:53], -1, 0
	v_readlane_b32 s12, v155, s59
	s_ashr_i32 s85, s84, 31
; #define GAS __attribute__((address_space(1)))
; __device__ __forceinline__ bf16_t* x_row_ptr(Frame& F, int row) { return (bf16_t*)(F.ws + WS_X) + (size_t)row * D; }
; __device__ __forceinline__ void rowrq_issue(Frame& F, RowRq& R, int row, unsigned ts) {
;     R.row = row; R.ts = ts;
;     const GAS u32x4* xr = (const GAS u32x4*)x_row_ptr(F, row) + 2 * F.lane;
;     R.x[0] = xr[0]; R.x[1] = xr[1];
;     unsigned long long mask = __ballot(ts != 0xFFFFu);
;     unsigned vm = 0u;
; #pragma unroll
;     for (int k = 0; k < 8; ++k) {
;         const bool has = mask != 0ull;
;         const int e = has ? __builtin_ctzll(mask) : 0;
;         const unsigned sl = (unsigned)__builtin_amdgcn_readlane((int)ts, e);
;         mask &= mask - 1ull;
;         R.w[k] = *y_row_ptr16(F, row, has ? e : 0, has ? sl : 0u);
;         vm |= has ? (1u << k) : 0u;
;     }
;     R.vm = vm; R.rest = mask;
; }
; __device__ __forceinline__ void rowrq_consume(Frame& F, const RowRq& R, f32x4 (&v)[4]) {
; #pragma unroll
;     for (int h = 0; h < 2; ++h) { const u32x4 x = R.x[h]; v[2 * h] = (f32x4){bf_lo(x.x), bf_hi(x.x), bf_lo(x.y), bf_hi(x.y)}; v[2 * h + 1] = (f32x4){bf_lo(x.z), bf_hi(x.z), bf_lo(x.w), bf_hi(x.w)}; }
; #pragma unroll
;     for (int k = 0; k < 8; ++k)
;         if ((R.vm >> k) & 1u) {
; #pragma unroll
;             for (int q = 0; q < 4; ++q) y_add4(v[q], R.w[k][q]); }
	global_load_dwordx4 v[146:149], v[166:167], off offset:16 nt
	global_load_dwordx4 v[150:153], v[166:167], off nt
	global_load_dwordx4 v[142:145], v154, s[88:89]
	global_load_dwordx4 v[138:141], v154, s[64:65]
	s_lshl_b64 s[60:61], s[84:85], 18
	s_lshl_b64 s[64:65], s[12:13], 10
	v_writelane_b32 v255, s52, 28
	s_and_b64 s[78:79], s[78:79], exec
	s_cselect_b32 s12, 0, s65
	v_writelane_b32 v255, s53, 29
	s_cselect_b32 s52, 0, s64
	s_add_u32 s53, s90, s60
	s_addc_u32 s59, s91, s61
	s_add_u32 s60, s53, s52
	s_addc_u32 s61, s59, s12
	s_cmp_lg_u64 s[34:35], 0
	s_cselect_b64 s[34:35], -1, 0
	v_writelane_b32 v255, s34, 30
	v_readlane_b32 s12, v155, s47
	s_ashr_i32 s77, s76, 31
	v_writelane_b32 v255, s35, 31
	s_lshl_b64 s[34:35], s[76:77], 18
	s_lshl_b64 s[76:77], s[12:13], 10
	s_and_b64 s[74:75], s[74:75], exec
	s_cselect_b32 s12, 0, s77
	s_cselect_b32 s47, 0, s76
	s_add_u32 s34, s90, s34
	s_addc_u32 s35, s91, s35
	s_add_u32 s34, s34, s47
	s_addc_u32 s35, s35, s12
	s_cmp_lg_u64 s[18:19], 0
	s_cselect_b64 s[18:19], -1, 0
	v_writelane_b32 v255, s18, 32
	v_readlane_b32 s12, v155, s45
	s_ashr_i32 s47, s46, 31
	global_load_dwordx4 v[134:137], v154, s[60:61]
	global_load_dwordx4 v[130:133], v154, s[34:35]
	v_writelane_b32 v255, s19, 33
	s_lshl_b64 s[18:19], s[46:47], 18
	s_lshl_b64 s[34:35], s[12:13], 10
	s_and_b64 s[46:47], s[62:63], exec
	s_cselect_b32 s12, 0, s35
	s_cselect_b32 s34, 0, s34
	s_add_u32 s18, s90, s18
	s_addc_u32 s19, s91, s19
	s_add_u32 s18, s18, s34
	s_addc_u32 s19, s19, s12
	s_cmp_lg_u64 s[22:23], 0
	s_cselect_b64 s[22:23], -1, 0
	v_writelane_b32 v255, s22, 34
	v_readlane_b32 s12, v155, s29
	s_ashr_i32 s59, s58, 31
	v_writelane_b32 v255, s23, 35
	s_lshl_b64 s[22:23], s[58:59], 18
	s_lshl_b64 s[34:35], s[12:13], 10
	s_and_b64 s[30:31], s[30:31], exec
	s_cselect_b32 s12, 0, s35
	s_cselect_b32 s29, 0, s34
	s_add_u32 s22, s90, s22
	s_addc_u32 s23, s91, s23
	s_add_u32 s22, s22, s29
	s_addc_u32 s23, s23, s12
	s_cmp_lg_u64 s[10:11], 0
	s_cselect_b64 s[10:11], -1, 0
	v_writelane_b32 v255, s10, 36
	v_readlane_b32 s12, v155, s25
	s_ashr_i32 s29, s28, 31
	global_load_dwordx4 v[126:129], v154, s[18:19]
	global_load_dwordx4 v[122:125], v154, s[22:23]
	v_writelane_b32 v255, s11, 37
	s_lshl_b64 s[10:11], s[28:29], 18
	s_lshl_b64 s[18:19], s[12:13], 10
	s_and_b64 s[6:7], s[6:7], exec
	s_cselect_b32 s7, 0, s19
	s_cselect_b32 s6, 0, s18
	s_add_u32 s10, s90, s10
	s_addc_u32 s11, s91, s11
	s_add_u32 s6, s10, s6
	s_addc_u32 s7, s11, s7
	s_cmp_lg_u64 s[56:57], 0
	s_cselect_b64 s[10:11], -1, 0
	v_writelane_b32 v255, s10, 38
	v_readlane_b32 s12, v155, s9
	s_ashr_i32 s9, s8, 31
	v_writelane_b32 v255, s11, 39
	s_lshl_b64 s[8:9], s[8:9], 18
	s_lshl_b64 s[10:11], s[12:13], 10
	s_and_b64 s[2:3], s[2:3], exec
	s_cselect_b32 s3, 0, s11
	s_cselect_b32 s2, 0, s10
	s_add_u32 s8, s90, s8
	s_addc_u32 s9, s91, s9
	s_add_u32 s2, s8, s2
	s_addc_u32 s3, s9, s3
	global_load_dwordx4 v[118:121], v154, s[6:7]
	global_load_dwordx4 v[114:117], v154, s[2:3]
	s_waitcnt vmcnt(28)
	v_lshlrev_b32_e32 v172, 16, v110
	v_and_b32_e32 v173, 0xffff0000, v110
	v_lshlrev_b32_e32 v174, 16, v111
	v_and_b32_e32 v175, 0xffff0000, v111
	v_lshlrev_b32_e32 v168, 16, v112
	v_and_b32_e32 v169, 0xffff0000, v112
	v_lshlrev_b32_e32 v170, 16, v113
	v_and_b32_e32 v171, 0xffff0000, v113
	v_lshlrev_b32_e32 v110, 16, v106
	v_and_b32_e32 v111, 0xffff0000, v106
	v_lshlrev_b32_e32 v112, 16, v107
	v_and_b32_e32 v113, 0xffff0000, v107
	v_lshlrev_b32_e32 v106, 16, v108
	v_and_b32_e32 v107, 0xffff0000, v108
	v_lshlrev_b32_e32 v108, 16, v109
	s_bitcmp0_b32 s5, 0
	v_and_b32_e32 v109, 0xffff0000, v109
	s_cbranch_scc1 .LBB0_224
	s_waitcnt vmcnt(27)
	v_cvt_f32_fp8_e32 v180, v102
	v_cvt_f32_fp8_sdwa v181, v102 src0_sel:BYTE_1
	v_pk_fma_f32 v[172:173], v[180:181], s[14:15], v[172:173] op_sel_hi:[1,0,1]
	v_cvt_f32_fp8_sdwa v180, v102 src0_sel:BYTE_2
	v_cvt_f32_fp8_sdwa v181, v102 src0_sel:BYTE_3
	v_cvt_f32_fp8_sdwa v102, v103 src0_sel:BYTE_2
	v_pk_fma_f32 v[174:175], v[180:181], s[14:15], v[174:175] op_sel_hi:[1,0,1]
	v_cvt_f32_fp8_e32 v180, v103
	v_cvt_f32_fp8_sdwa v181, v103 src0_sel:BYTE_1
	v_cvt_f32_fp8_sdwa v103, v103 src0_sel:BYTE_3
	v_pk_fma_f32 v[168:169], v[180:181], s[14:15], v[168:169] op_sel_hi:[1,0,1]
	v_pk_fma_f32 v[170:171], v[102:103], s[14:15], v[170:171] op_sel_hi:[1,0,1]
	v_cvt_f32_fp8_e32 v102, v104
	v_cvt_f32_fp8_sdwa v103, v104 src0_sel:BYTE_1
	v_pk_fma_f32 v[110:111], v[102:103], s[14:15], v[110:111] op_sel_hi:[1,0,1]
	v_cvt_f32_fp8_sdwa v102, v104 src0_sel:BYTE_2
	v_cvt_f32_fp8_sdwa v103, v104 src0_sel:BYTE_3
	v_pk_fma_f32 v[112:113], v[102:103], s[14:15], v[112:113] op_sel_hi:[1,0,1]
	v_cvt_f32_fp8_e32 v102, v105
	v_cvt_f32_fp8_sdwa v103, v105 src0_sel:BYTE_1
	v_pk_fma_f32 v[106:107], v[102:103], s[14:15], v[106:107] op_sel_hi:[1,0,1]
	v_cvt_f32_fp8_sdwa v102, v105 src0_sel:BYTE_2
	v_cvt_f32_fp8_sdwa v103, v105 src0_sel:BYTE_3
	v_pk_fma_f32 v[108:109], v[102:103], s[14:15], v[108:109] op_sel_hi:[1,0,1]
	s_bitcmp0_b32 s5, 1
	s_cbranch_scc0 .LBB0_225

; #define GAS __attribute__((address_space(1)))
; __device__ __forceinline__ bf16_t* x_row_ptr(Frame& F, int row) { return (bf16_t*)(F.ws + WS_X) + (size_t)row * D; }
; __device__ __forceinline__ void rowrq_issue(Frame& F, RowRq& R, int row, unsigned ts) {
;     R.row = row; R.ts = ts;
;     const GAS u32x4* xr = (const GAS u32x4*)x_row_ptr(F, row) + 2 * F.lane;
;     R.x[0] = xr[0]; R.x[1] = xr[1];
;     unsigned long long mask = __ballot(ts != 0xFFFFu);
;     unsigned vm = 0u;
; #pragma unroll
;     for (int k = 0; k < 8; ++k) {
;         const bool has = mask != 0ull;
;         const int e = has ? __builtin_ctzll(mask) : 0;
;         const unsigned sl = (unsigned)__builtin_amdgcn_readlane((int)ts, e);
;         mask &= mask - 1ull;
;         R.w[k] = *y_row_ptr16(F, row, has ? e : 0, has ? sl : 0u);
;         vm |= has ? (1u << k) : 0u;
;     }
;     R.vm = vm; R.rest = mask;
; }
; __device__ __forceinline__ void rowrq_consume(Frame& F, const RowRq& R, f32x4 (&v)[4]) {
; #pragma unroll
;     for (int h = 0; h < 2; ++h) { const u32x4 x = R.x[h]; v[2 * h] = (f32x4){bf_lo(x.x), bf_hi(x.x), bf_lo(x.y), bf_hi(x.y)}; v[2 * h + 1] = (f32x4){bf_lo(x.z), bf_hi(x.z), bf_lo(x.w), bf_hi(x.w)}; }
; #pragma unroll
;     for (int k = 0; k < 8; ++k)
;         if ((R.vm >> k) & 1u) {
; #pragma unroll
;             for (int q = 0; q < 4; ++q) y_add4(v[q], R.w[k][q]); }
.LBB0_240:
	s_add_i32 s25, s33, 3
	v_readlane_b32 s0, v255, 25
	s_min_i32 s2, s25, s0
	v_mov_b32_e32 v177, 0xffff
	s_and_saveexec_b64 s[0:1], s[36:37]
	v_lshl_add_u32 v62, s2, 5, v178
	ds_read_u16 v177, v62
	s_or_b64 exec, exec, s[0:1]
	s_add_i32 s44, s2, s38
	s_mov_b32 s0, 0xffff
	s_waitcnt lgkmcnt(0)
	v_cmp_ne_u32_e32 vcc, s0, v177
	s_add_i32 s0, s44, 0xffff8000
	s_lshr_b32 s0, s0, 11
	s_add_i32 s12, s0, 0x100
	s_ashr_i32 s29, s44, 11
	s_add_u32 s0, vcc_lo, -1
	s_addc_u32 s1, vcc_hi, -1
	s_and_b64 s[4:5], s[0:1], vcc
	s_add_u32 s0, s4, -1
	s_addc_u32 s1, s5, -1
	s_and_b64 s[10:11], s[0:1], s[4:5]
	s_add_u32 s0, s10, -1
	s_addc_u32 s1, s11, -1
	s_and_b64 s[22:23], s[0:1], s[10:11]
	s_add_u32 s0, s22, -1
	s_addc_u32 s1, s23, -1
	s_and_b64 s[18:19], s[0:1], s[22:23]
	s_add_u32 s0, s18, -1
	s_addc_u32 s1, s19, -1
	s_and_b64 s[8:9], s[0:1], s[18:19]
	s_add_u32 s0, s8, -1
	s_addc_u32 s1, s9, -1
	s_and_b64 s[0:1], s[0:1], s[8:9]
	s_cmp_eq_u64 s[0:1], 0
	s_cselect_b64 s[76:77], -1, 0
	s_ff1_i32_b64 s6, s[0:1]
	s_and_b64 s[2:3], s[76:77], exec
	s_cselect_b32 s7, 0, s6
	s_add_u32 s2, s0, -1
	s_addc_u32 s3, s1, -1
	s_and_b64 s[0:1], s[2:3], s[0:1]
	s_lshl_b32 s2, s7, 4
	s_add_i32 s6, s2, s29
	s_lshl_b32 s28, s7, 1
	s_cmp_eq_u64 s[0:1], 0
	s_cselect_b64 s[74:75], -1, 0
	s_ff1_i32_b64 s30, s[0:1]
	s_and_b64 s[2:3], s[74:75], exec
	s_cselect_b32 s3, 0, s30
	s_lshl_b32 s2, s3, 4
	s_lshl_b32 s30, s3, 1
	s_add_i32 s2, s2, s29
	s_add_i32 s30, s30, s12
	s_cmp_lt_i32 s44, 0x8000
	s_cselect_b32 s2, s2, s30
	s_add_i32 s28, s28, s12
	s_cmp_lt_i32 s44, 0x8000
	s_cselect_b32 s6, s6, s28
	s_cmp_eq_u64 s[8:9], 0
	s_cselect_b64 s[34:35], -1, 0
	s_ff1_i32_b64 s28, s[8:9]
	s_and_b64 s[8:9], s[34:35], exec
	s_cselect_b32 s9, 0, s28
	s_lshl_b32 s8, s9, 4
	s_lshl_b32 s28, s9, 1
	s_add_i32 s8, s8, s29
	s_add_i32 s28, s28, s12
	s_cmp_lt_i32 s44, 0x8000
	s_cselect_b32 s8, s8, s28
	s_cmp_eq_u64 s[18:19], 0
	s_cselect_b64 s[84:85], -1, 0
	s_ff1_i32_b64 s28, s[18:19]
	s_and_b64 s[18:19], s[84:85], exec
	s_cselect_b32 s19, 0, s28
	s_lshl_b32 s18, s19, 4
	s_lshl_b32 s28, s19, 1
	s_add_i32 s18, s18, s29
	s_add_i32 s28, s28, s12
	s_cmp_lt_i32 s44, 0x8000
	s_cselect_b32 s18, s18, s28
	s_cmp_eq_u64 s[22:23], 0
	s_cselect_b64 s[88:89], -1, 0
	s_ff1_i32_b64 s28, s[22:23]
	s_and_b64 s[22:23], s[88:89], exec
	s_cselect_b32 s52, 0, s28
	s_lshl_b32 s22, s52, 4
	s_lshl_b32 s23, s52, 1
	s_add_i32 s22, s22, s29
	s_add_i32 s23, s23, s12
	s_cmp_lt_i32 s44, 0x8000
	s_cselect_b32 s28, s22, s23
	s_cmp_eq_u64 s[10:11], 0
	s_cselect_b64 s[22:23], -1, 0
	s_ff1_i32_b64 s30, s[10:11]
	s_and_b64 s[10:11], s[22:23], exec
	s_cselect_b32 s31, 0, s30
	s_lshl_b32 s10, s31, 4
	s_lshl_b32 s11, s31, 1
	s_add_i32 s10, s10, s29
	s_add_i32 s11, s11, s12
	s_cmp_lt_i32 s44, 0x8000
	s_cselect_b32 s30, s10, s11
	s_cmp_eq_u64 s[4:5], 0
	s_cselect_b64 s[10:11], -1, 0
	s_ff1_i32_b64 s45, s[4:5]
	s_and_b64 s[4:5], s[10:11], exec
	s_cselect_b32 s47, 0, s45
	s_lshl_b32 s4, s47, 4
	s_lshl_b32 s5, s47, 1
	s_add_i32 s4, s4, s29
	s_add_i32 s5, s5, s12
	s_cmp_lt_i32 s44, 0x8000
	s_cselect_b32 s46, s4, s5
	s_cmp_lg_u64 vcc, 0
	s_cselect_b64 s[4:5], -1, 0
	s_ff1_i32_b64 s45, vcc
	s_and_b64 s[58:59], s[4:5], exec
	s_cselect_b32 s53, s45, 0
	s_lshl_b32 s45, s53, 4
	s_add_i32 s45, s45, s29
	s_lshl_b32 s29, s53, 1
	s_add_i32 s29, s29, s12
	s_cmp_lt_i32 s44, 0x8000
	s_cselect_b32 s58, s45, s29
	s_ashr_i32 s45, s44, 31
	s_lshl_b64 s[60:61], s[44:45], 11
	v_readlane_b32 s12, v177, s53
	s_ashr_i32 s59, s58, 31
	v_lshl_add_u64 v[62:63], v[160:161], 0, s[60:61]
	s_lshl_b64 s[58:59], s[58:59], 18
	s_lshl_b64 s[60:61], s[12:13], 10
	s_and_b64 s[78:79], s[4:5], exec
	s_cselect_b32 s12, s61, 0
	s_cselect_b32 s29, s60, 0
	s_add_u32 s45, s90, s58
	s_addc_u32 s53, s91, s59
	s_add_u32 s58, s45, s29
	s_addc_u32 s59, s53, s12
	v_readlane_b32 s12, v177, s47
	s_ashr_i32 s47, s46, 31
	s_lshl_b64 s[46:47], s[46:47], 18
	s_lshl_b64 s[60:61], s[12:13], 10
	s_and_b64 s[78:79], s[10:11], exec
	s_cselect_b32 s12, 0, s61
	s_cselect_b32 s29, 0, s60
	s_add_u32 s45, s90, s46
	s_addc_u32 s47, s91, s47
	s_add_u32 s46, s45, s29
	s_addc_u32 s47, s47, s12
	v_readlane_b32 s12, v177, s31
	s_ashr_i32 s31, s30, 31
	global_load_dwordx4 v[106:109], v[62:63], off offset:16 nt
	global_load_dwordx4 v[110:113], v[62:63], off nt
	global_load_dwordx4 v[102:105], v154, s[58:59]
	global_load_dwordx4 v[98:101], v154, s[46:47]
	s_lshl_b64 s[30:31], s[30:31], 18
	s_lshl_b64 s[46:47], s[12:13], 10
	s_and_b64 s[58:59], s[22:23], exec
	s_cselect_b32 s12, 0, s47
	s_cselect_b32 s29, 0, s46
	s_add_u32 s30, s90, s30
	s_addc_u32 s31, s91, s31
	s_add_u32 s30, s30, s29
	s_addc_u32 s31, s31, s12
	v_readlane_b32 s12, v177, s52
	s_ashr_i32 s29, s28, 31
	s_lshl_b64 s[28:29], s[28:29], 18
	s_lshl_b64 s[46:47], s[12:13], 10
	s_and_b64 s[58:59], s[88:89], exec
	s_cselect_b32 s12, 0, s47
	s_cselect_b32 s45, 0, s46
	s_add_u32 s28, s90, s28
	s_addc_u32 s29, s91, s29
	s_add_u32 s28, s28, s45
	s_addc_u32 s29, s29, s12
	v_readlane_b32 s12, v177, s19
	s_ashr_i32 s19, s18, 31
	global_load_dwordx4 v[94:97], v154, s[30:31]
	global_load_dwordx4 v[90:93], v154, s[28:29]
	s_lshl_b64 s[18:19], s[18:19], 18
	s_lshl_b64 s[28:29], s[12:13], 10
	s_and_b64 s[30:31], s[84:85], exec
	s_cselect_b32 s12, 0, s29
	s_cselect_b32 s28, 0, s28
	s_add_u32 s18, s90, s18
	s_addc_u32 s19, s91, s19
	s_add_u32 s18, s18, s28
	s_addc_u32 s19, s19, s12
	v_readlane_b32 s12, v177, s9
	s_ashr_i32 s9, s8, 31
	s_lshl_b64 s[8:9], s[8:9], 18
	s_lshl_b64 s[28:29], s[12:13], 10
	s_and_b64 s[30:31], s[34:35], exec
	s_cselect_b32 s12, 0, s29
	s_cselect_b32 s28, 0, s28
	s_add_u32 s8, s90, s8
	s_addc_u32 s9, s91, s9
	s_add_u32 s8, s8, s28
	s_addc_u32 s9, s9, s12
	v_readlane_b32 s12, v177, s7
	s_ashr_i32 s7, s6, 31
	global_load_dwordx4 v[86:89], v154, s[18:19]
	global_load_dwordx4 v[82:85], v154, s[8:9]
	s_lshl_b64 s[6:7], s[6:7], 18
	s_lshl_b64 s[8:9], s[12:13], 10
	s_and_b64 s[18:19], s[76:77], exec
	s_cselect_b32 s9, 0, s9
	s_cselect_b32 s8, 0, s8
	s_add_u32 s6, s90, s6
	s_addc_u32 s7, s91, s7
	s_add_u32 s6, s6, s8
	s_addc_u32 s7, s7, s9
	v_readlane_b32 s12, v177, s3
	s_ashr_i32 s3, s2, 31
	s_lshl_b64 s[2:3], s[2:3], 18
	s_lshl_b64 s[8:9], s[12:13], 10
	s_and_b64 s[18:19], s[74:75], exec
	s_cselect_b32 s9, 0, s9
	s_cselect_b32 s8, 0, s8
	s_add_u32 s2, s90, s2
	s_addc_u32 s3, s91, s3
	s_add_u32 s2, s2, s8
	s_addc_u32 s3, s3, s9
	global_load_dwordx4 v[78:81], v154, s[6:7]
	global_load_dwordx4 v[62:65], v154, s[2:3]
	s_waitcnt vmcnt(30)
	v_lshlrev_b32_e32 v172, 16, v74
	v_and_b32_e32 v173, 0xffff0000, v74
	v_lshlrev_b32_e32 v174, 16, v75
	v_and_b32_e32 v175, 0xffff0000, v75
	v_lshlrev_b32_e32 v168, 16, v76
	v_and_b32_e32 v169, 0xffff0000, v76
	v_lshlrev_b32_e32 v170, 16, v77
	v_and_b32_e32 v171, 0xffff0000, v77
	v_lshlrev_b32_e32 v74, 16, v70
	v_and_b32_e32 v75, 0xffff0000, v70
	v_lshlrev_b32_e32 v76, 16, v71
	v_and_b32_e32 v77, 0xffff0000, v71
	v_lshlrev_b32_e32 v70, 16, v72
	v_and_b32_e32 v71, 0xffff0000, v72
	v_lshlrev_b32_e32 v72, 16, v73
	s_bitcmp0_b32 s41, 0
	v_and_b32_e32 v73, 0xffff0000, v73
	s_cbranch_scc1 .LBB0_251
; __device__ __forceinline__ void y_add4(f32x4& v, unsigned w) {
;     constexpr float r = 1.0f / pg8::SC_Y;
;     v[0] += __builtin_amdgcn_cvt_f32_fp8((int)w, 0) * r; v[1] += __builtin_amdgcn_cvt_f32_fp8((int)w, 1) * r; v[2] += __builtin_amdgcn_cvt_f32_fp8((int)w, 2) * r; v[3] += __builtin_amdgcn_cvt_f32_fp8((int)w, 3) * r;
; }
; __device__ __forceinline__ void rowrq_consume(Frame& F, const RowRq& R, f32x4 (&v)[4]) {
;     ...
; #pragma unroll
;     for (int k = 0; k < 8; ++k)
;         if ((R.vm >> k) & 1u) {
; #pragma unroll
;             for (int q = 0; q < 4; ++q) y_add4(v[q], R.w[k][q]); }
	s_waitcnt vmcnt(29)
	v_cvt_f32_fp8_e32 v184, v66
	v_cvt_f32_fp8_sdwa v185, v66 src0_sel:BYTE_1
	v_pk_fma_f32 v[172:173], v[184:185], s[14:15], v[172:173] op_sel_hi:[1,0,1]
	v_cvt_f32_fp8_sdwa v184, v66 src0_sel:BYTE_2
	v_cvt_f32_fp8_sdwa v185, v66 src0_sel:BYTE_3
	v_cvt_f32_fp8_sdwa v66, v67 src0_sel:BYTE_2
	v_pk_fma_f32 v[174:175], v[184:185], s[14:15], v[174:175] op_sel_hi:[1,0,1]
	v_cvt_f32_fp8_e32 v184, v67
	v_cvt_f32_fp8_sdwa v185, v67 src0_sel:BYTE_1
	v_cvt_f32_fp8_sdwa v67, v67 src0_sel:BYTE_3
	v_pk_fma_f32 v[168:169], v[184:185], s[14:15], v[168:169] op_sel_hi:[1,0,1]
	v_pk_fma_f32 v[170:171], v[66:67], s[14:15], v[170:171] op_sel_hi:[1,0,1]
	v_cvt_f32_fp8_e32 v66, v68
	v_cvt_f32_fp8_sdwa v67, v68 src0_sel:BYTE_1
	v_pk_fma_f32 v[74:75], v[66:67], s[14:15], v[74:75] op_sel_hi:[1,0,1]
	v_cvt_f32_fp8_sdwa v66, v68 src0_sel:BYTE_2
	v_cvt_f32_fp8_sdwa v67, v68 src0_sel:BYTE_3
	v_pk_fma_f32 v[76:77], v[66:67], s[14:15], v[76:77] op_sel_hi:[1,0,1]
	v_cvt_f32_fp8_e32 v66, v69
	v_cvt_f32_fp8_sdwa v67, v69 src0_sel:BYTE_1
	v_pk_fma_f32 v[70:71], v[66:67], s[14:15], v[70:71] op_sel_hi:[1,0,1]
	v_cvt_f32_fp8_sdwa v66, v69 src0_sel:BYTE_2
	v_cvt_f32_fp8_sdwa v67, v69 src0_sel:BYTE_3
	v_pk_fma_f32 v[72:73], v[66:67], s[14:15], v[72:73] op_sel_hi:[1,0,1]
	s_bitcmp0_b32 s41, 1
	s_cbranch_scc0 .LBB0_252

; #define GAS __attribute__((address_space(1)))
; __device__ __forceinline__ bf16_t* x_row_ptr(Frame& F, int row) { return (bf16_t*)(F.ws + WS_X) + (size_t)row * D; }
; __device__ __forceinline__ void rowrq_issue(Frame& F, RowRq& R, int row, unsigned ts) {
;     R.row = row; R.ts = ts;
;     const GAS u32x4* xr = (const GAS u32x4*)x_row_ptr(F, row) + 2 * F.lane;
;     R.x[0] = xr[0]; R.x[1] = xr[1];
;     unsigned long long mask = __ballot(ts != 0xFFFFu);
;     unsigned vm = 0u;
; #pragma unroll
;     for (int k = 0; k < 8; ++k) {
;         const bool has = mask != 0ull;
;         const int e = has ? __builtin_ctzll(mask) : 0;
;         const unsigned sl = (unsigned)__builtin_amdgcn_readlane((int)ts, e);
;         mask &= mask - 1ull;
;         R.w[k] = *y_row_ptr16(F, row, has ? e : 0, has ? sl : 0u);
;         vm |= has ? (1u << k) : 0u;
;     }
;     R.vm = vm; R.rest = mask;
; }
.LBB0_265:
	s_add_i32 s2, s33, 4
	v_readlane_b32 s3, v255, 25
	s_min_i32 s6, s2, s3
	v_mov_b32_e32 v176, 0xffff
	s_and_saveexec_b64 s[2:3], s[36:37]
	v_lshl_add_u32 v34, s6, 5, v178
	ds_read_u16 v176, v34
	s_or_b64 exec, exec, s[2:3]
	s_add_i32 s40, s6, s38
	s_mov_b32 s2, 0xffff
	s_waitcnt lgkmcnt(0)
	v_cmp_ne_u32_e32 vcc, s2, v176
	s_add_i32 s2, s40, 0xffff8000
	s_lshr_b32 s2, s2, 11
	s_add_i32 s12, s2, 0x100
	s_ashr_i32 s41, s40, 11
	s_add_u32 s2, vcc_lo, -1
	s_addc_u32 s3, vcc_hi, -1
	s_and_b64 s[2:3], s[2:3], vcc
	s_add_u32 s6, s2, -1
	s_addc_u32 s7, s3, -1
	s_and_b64 s[8:9], s[6:7], s[2:3]
	s_add_u32 s6, s8, -1
	s_addc_u32 s7, s9, -1
	s_and_b64 s[28:29], s[6:7], s[8:9]
	s_add_u32 s6, s28, -1
	s_addc_u32 s7, s29, -1
	s_and_b64 s[6:7], s[6:7], s[28:29]
	s_add_u32 s18, s6, -1
	s_addc_u32 s19, s7, -1
	s_and_b64 s[46:47], s[18:19], s[6:7]
	s_add_u32 s18, s46, -1
	s_addc_u32 s19, s47, -1
	s_and_b64 s[18:19], s[18:19], s[46:47]
	s_cmp_eq_u64 s[18:19], 0
	s_cselect_b64 s[30:31], -1, 0
	s_ff1_i32_b64 s45, s[18:19]
	s_and_b64 s[42:43], s[30:31], exec
	s_cselect_b32 s45, 0, s45
	s_add_u32 s42, s18, -1
	s_addc_u32 s43, s19, -1
	s_and_b64 s[42:43], s[42:43], s[18:19]
	s_lshl_b32 s18, s45, 4
	s_add_i32 s52, s18, s41
	s_lshl_b32 s53, s45, 1
	s_cmp_eq_u64 s[42:43], 0
	s_cselect_b64 s[86:87], -1, 0
	s_ff1_i32_b64 s58, s[42:43]
	s_and_b64 s[18:19], s[86:87], exec
	s_cselect_b32 s19, 0, s58
	s_lshl_b32 s18, s19, 4
	s_lshl_b32 s58, s19, 1
	s_add_i32 s18, s18, s41
	s_add_i32 s58, s58, s12
	s_cmp_lt_i32 s40, 0x8000
	s_cselect_b32 s18, s18, s58
	s_add_i32 s53, s53, s12
	s_cmp_lt_i32 s40, 0x8000
	s_cselect_b32 s92, s52, s53
	s_cmp_eq_u64 s[46:47], 0
	s_cselect_b64 s[94:95], -1, 0
	s_ff1_i32_b64 s52, s[46:47]
	s_and_b64 s[46:47], s[94:95], exec
	s_cselect_b32 s47, 0, s52
	s_lshl_b32 s46, s47, 4
	s_lshl_b32 s52, s47, 1
	s_add_i32 s46, s46, s41
	s_add_i32 s52, s52, s12
	s_cmp_lt_i32 s40, 0x8000
	s_cselect_b32 s46, s46, s52
	s_cmp_eq_u64 s[6:7], 0
	s_cselect_b64 s[78:79], -1, 0
	s_ff1_i32_b64 s52, s[6:7]
	s_and_b64 s[6:7], s[78:79], exec
	s_cselect_b32 s59, 0, s52
	s_lshl_b32 s6, s59, 4
	s_lshl_b32 s7, s59, 1
	s_add_i32 s6, s6, s41
	s_add_i32 s7, s7, s12
	s_cmp_lt_i32 s40, 0x8000
	s_cselect_b32 s58, s6, s7
	s_cmp_eq_u64 s[28:29], 0
	s_cselect_b64 s[6:7], -1, 0
	s_ff1_i32_b64 s52, s[28:29]
	s_and_b64 s[28:29], s[6:7], exec
	s_cselect_b32 s61, 0, s52
	s_lshl_b32 s28, s61, 4
	s_lshl_b32 s29, s61, 1
	s_add_i32 s28, s28, s41
	s_add_i32 s29, s29, s12
	s_cmp_lt_i32 s40, 0x8000
	s_cselect_b32 s60, s28, s29
	s_cmp_eq_u64 s[8:9], 0
	s_cselect_b64 s[28:29], -1, 0
	s_ff1_i32_b64 s52, s[8:9]
	s_and_b64 s[8:9], s[28:29], exec
	s_cselect_b32 s63, 0, s52
	s_lshl_b32 s8, s63, 4
	s_lshl_b32 s9, s63, 1
	s_add_i32 s8, s8, s41
	s_add_i32 s9, s9, s12
	s_cmp_lt_i32 s40, 0x8000
	s_cselect_b32 s62, s8, s9
	s_cmp_eq_u64 s[2:3], 0
	s_cselect_b64 s[8:9], -1, 0
	s_ff1_i32_b64 s52, s[2:3]
	s_and_b64 s[2:3], s[8:9], exec
	s_cselect_b32 s65, 0, s52
	s_lshl_b32 s2, s65, 4
	s_lshl_b32 s3, s65, 1
	s_add_i32 s2, s2, s41
	s_add_i32 s3, s3, s12
	s_cmp_lt_i32 s40, 0x8000
	s_cselect_b32 s64, s2, s3
	s_cmp_lg_u64 vcc, 0
	s_cselect_b64 s[2:3], -1, 0
	s_ff1_i32_b64 s52, vcc
	s_and_b64 vcc, s[2:3], exec
	s_cselect_b32 s52, s52, 0
	s_lshl_b32 s53, s52, 4
	s_add_i32 s53, s53, s41
	s_lshl_b32 s41, s52, 1
	s_add_i32 s41, s41, s12
	s_cmp_lt_i32 s40, 0x8000
	s_cselect_b32 vcc_lo, s53, s41
	s_ashr_i32 s41, s40, 31
	s_lshl_b64 s[68:69], s[40:41], 11
	v_readlane_b32 s12, v176, s52
	s_ashr_i32 vcc_hi, vcc_lo, 31
	v_lshl_add_u64 v[34:35], v[160:161], 0, s[68:69]
	s_lshl_b64 s[68:69], vcc, 18
	s_lshl_b64 vcc, s[12:13], 10
	s_and_b64 s[52:53], s[2:3], exec
	s_cselect_b32 s12, vcc_hi, 0
	s_cselect_b32 s41, vcc_lo, 0
	s_add_u32 s52, s90, s68
	s_addc_u32 s53, s91, s69
	s_add_u32 s52, s52, s41
	s_addc_u32 s53, s53, s12
	v_readlane_b32 s12, v176, s65
	s_ashr_i32 s65, s64, 31
	s_lshl_b64 s[64:65], s[64:65], 18
	s_lshl_b64 s[68:69], s[12:13], 10
	s_and_b64 vcc, s[8:9], exec
	s_cselect_b32 s12, 0, s69
	s_cselect_b32 s41, 0, s68
	s_add_u32 s64, s90, s64
	s_addc_u32 s65, s91, s65
	s_add_u32 s64, s64, s41
	s_addc_u32 s65, s65, s12
	v_readlane_b32 s12, v176, s63
	s_ashr_i32 s63, s62, 31
	global_load_dwordx4 v[70:73], v[34:35], off offset:16 nt
	global_load_dwordx4 v[74:77], v[34:35], off nt
	global_load_dwordx4 v[66:69], v154, s[52:53]
	global_load_dwordx4 v[58:61], v154, s[64:65]
	s_lshl_b64 s[52:53], s[62:63], 18
	s_lshl_b64 s[62:63], s[12:13], 10
	s_and_b64 s[64:65], s[28:29], exec
	s_cselect_b32 s12, 0, s63
	s_cselect_b32 s41, 0, s62
	s_add_u32 s52, s90, s52
	s_addc_u32 s53, s91, s53
	s_add_u32 s52, s52, s41
	s_addc_u32 s53, s53, s12
	v_readlane_b32 s12, v176, s61
	s_ashr_i32 s61, s60, 31
	s_lshl_b64 s[60:61], s[60:61], 18
	s_lshl_b64 s[62:63], s[12:13], 10
	s_and_b64 s[64:65], s[6:7], exec
	s_cselect_b32 s12, 0, s63
	s_cselect_b32 s41, 0, s62
	s_add_u32 s60, s90, s60
	s_addc_u32 s61, s91, s61
	s_add_u32 s60, s60, s41
	s_addc_u32 s61, s61, s12
	v_readlane_b32 s12, v176, s59
	s_ashr_i32 s59, s58, 31
	global_load_dwordx4 v[54:57], v154, s[52:53]
	global_load_dwordx4 v[50:53], v154, s[60:61]
	s_lshl_b64 s[52:53], s[58:59], 18
	s_lshl_b64 s[58:59], s[12:13], 10
	s_and_b64 s[60:61], s[78:79], exec
	s_cselect_b32 s12, 0, s59
	s_cselect_b32 s41, 0, s58
	s_add_u32 s52, s90, s52
	s_addc_u32 s53, s91, s53
	s_add_u32 s52, s52, s41
	s_addc_u32 s53, s53, s12
	v_readlane_b32 s12, v176, s47
	s_ashr_i32 s47, s46, 31
	s_lshl_b64 s[46:47], s[46:47], 18
	s_lshl_b64 s[58:59], s[12:13], 10
	s_and_b64 s[60:61], s[94:95], exec
	s_cselect_b32 s12, 0, s59
	s_cselect_b32 s41, 0, s58
	s_add_u32 s46, s90, s46
	s_addc_u32 s47, s91, s47
	s_add_u32 s46, s46, s41
	s_addc_u32 s47, s47, s12
	v_readlane_b32 s12, v176, s45
	s_ashr_i32 s93, s92, 31
	global_load_dwordx4 v[46:49], v154, s[52:53]
	global_load_dwordx4 v[42:45], v154, s[46:47]
	s_lshl_b64 s[46:47], s[92:93], 18
	s_lshl_b64 s[52:53], s[12:13], 10
	s_and_b64 s[58:59], s[30:31], exec
	s_cselect_b32 s12, 0, s53
	s_cselect_b32 s41, 0, s52
	s_add_u32 s45, s90, s46
	s_addc_u32 s47, s91, s47
	s_add_u32 s46, s45, s41
	s_addc_u32 s47, s47, s12
	v_readlane_b32 s12, v176, s19
	s_ashr_i32 s19, s18, 31
	s_lshl_b64 s[18:19], s[18:19], 18
	s_lshl_b64 s[52:53], s[12:13], 10
	s_and_b64 s[58:59], s[86:87], exec
	s_cselect_b32 s12, 0, s53
	s_cselect_b32 s41, 0, s52
	s_add_u32 s18, s90, s18
	s_addc_u32 s19, s91, s19
	s_add_u32 s18, s18, s41
	s_addc_u32 s19, s19, s12
	global_load_dwordx4 v[38:41], v154, s[46:47]
	global_load_dwordx4 v[34:37], v154, s[18:19]
	s_waitcnt vmcnt(32)
; __device__ __forceinline__ void rowrq_consume(Frame& F, const RowRq& R, f32x4 (&v)[4]) {
;     ...
;     for (int h = 0; h < 2; ++h) { const u32x4 x = R.x[h]; v[2 * h] = (f32x4){bf_lo(x.x), bf_hi(x.x), bf_lo(x.y), bf_hi(x.y)}; v[2 * h + 1] = (f32x4){bf_lo(x.z), bf_hi(x.z), bf_lo(x.w), bf_hi(x.w)}; }
; #pragma unroll
;     for (int k = 0; k < 8; ++k)
;         if ((R.vm >> k) & 1u) {
; #pragma unroll
;             for (int q = 0; q < 4; ++q) y_add4(v[q], R.w[k][q]); }
	v_lshlrev_b32_e32 v172, 16, v150
	v_and_b32_e32 v173, 0xffff0000, v150
	v_lshlrev_b32_e32 v174, 16, v151
	v_and_b32_e32 v175, 0xffff0000, v151
	v_lshlrev_b32_e32 v168, 16, v152
	v_and_b32_e32 v169, 0xffff0000, v152
	v_lshlrev_b32_e32 v170, 16, v153
	v_and_b32_e32 v171, 0xffff0000, v153
	v_lshlrev_b32_e32 v150, 16, v146
	v_and_b32_e32 v151, 0xffff0000, v146
	v_lshlrev_b32_e32 v152, 16, v147
	v_and_b32_e32 v153, 0xffff0000, v147
	v_lshlrev_b32_e32 v146, 16, v148
	v_and_b32_e32 v147, 0xffff0000, v148
	v_lshlrev_b32_e32 v148, 16, v149
	s_andn2_b64 vcc, exec, s[72:73]
	v_and_b32_e32 v149, 0xffff0000, v149
	s_cbranch_vccnz .LBB0_269
	s_waitcnt vmcnt(31)
	v_cvt_f32_fp8_e32 v184, v142
	v_cvt_f32_fp8_sdwa v185, v142 src0_sel:BYTE_1
	v_pk_fma_f32 v[172:173], v[184:185], s[14:15], v[172:173] op_sel_hi:[1,0,1]
	v_cvt_f32_fp8_sdwa v184, v142 src0_sel:BYTE_2
	v_cvt_f32_fp8_sdwa v185, v142 src0_sel:BYTE_3
	v_cvt_f32_fp8_sdwa v142, v143 src0_sel:BYTE_2
	v_pk_fma_f32 v[174:175], v[184:185], s[14:15], v[174:175] op_sel_hi:[1,0,1]
	v_cvt_f32_fp8_e32 v184, v143
	v_cvt_f32_fp8_sdwa v185, v143 src0_sel:BYTE_1
	v_cvt_f32_fp8_sdwa v143, v143 src0_sel:BYTE_3
	v_pk_fma_f32 v[168:169], v[184:185], s[14:15], v[168:169] op_sel_hi:[1,0,1]
	v_pk_fma_f32 v[170:171], v[142:143], s[14:15], v[170:171] op_sel_hi:[1,0,1]
	v_cvt_f32_fp8_e32 v142, v144
	v_cvt_f32_fp8_sdwa v143, v144 src0_sel:BYTE_1
	v_pk_fma_f32 v[150:151], v[142:143], s[14:15], v[150:151] op_sel_hi:[1,0,1]
	v_cvt_f32_fp8_sdwa v142, v144 src0_sel:BYTE_2
	v_cvt_f32_fp8_sdwa v143, v144 src0_sel:BYTE_3
	v_pk_fma_f32 v[152:153], v[142:143], s[14:15], v[152:153] op_sel_hi:[1,0,1]
	v_cvt_f32_fp8_e32 v142, v145
	v_cvt_f32_fp8_sdwa v143, v145 src0_sel:BYTE_1
	v_pk_fma_f32 v[146:147], v[142:143], s[14:15], v[146:147] op_sel_hi:[1,0,1]
	v_cvt_f32_fp8_sdwa v142, v145 src0_sel:BYTE_2
	v_cvt_f32_fp8_sdwa v143, v145 src0_sel:BYTE_3
	v_pk_fma_f32 v[148:149], v[142:143], s[14:15], v[148:149] op_sel_hi:[1,0,1]

; #define GAS __attribute__((address_space(1)))
; #define LAS __attribute__((address_space(3)))
; __device__ __forceinline__ void n2_phase(const Frame& F0, int L, int nrows) {
;     ...
;     { const GAS u32x4* img = (const GAS u32x4*)(F.ws + WS_RIMG + (size_t)L * 65536) + F.tid;
;       u32x4 iv[8];
; #pragma unroll
;       for (int i = 0; i < 8; ++i) iv[i] = img[512 * i];
; #pragma unroll
;       for (int i = 0; i < 8; ++i) *((LAS u32x4*)WH + F.tid + 512 * i) = iv[i]; }
;     __syncthreads();
;     const float* gn = inp(F, I_N2G) + L * 1024; const float* modL = (const float*)(F.ws + WS_MOD) + (size_t)L * 17 * 6144;
;     unsigned char* H8 = F.ws + WS_H; float* AFF = (float*)(F.ws + WS_AFF); const bf16_t* X = (const bf16_t*)(F.ws + WS_X);
;     const int RPB = nrows / F.G, NG = RPB / 16, rb = (int)blockIdx.x * RPB;
;     const int r = F.lane & 15, kg = F.lane >> 4, c0 = 128 * F.wave + 8 * kg;
;     u32x4 nraw[4];
; #pragma unroll
;     for (int s_ = 0; s_ < 4; ++s_) nraw[s_] = *(const GAS u32x4*)(X + (size_t)(rb + r) * D + c0 + 32 * s_);
.LBB0_1200:
	s_andn2_b64 vcc, exec, s[0:1]
	s_cbranch_vccnz .LBB0_1268
	v_readlane_b32 s0, v255, 17
	v_readlane_b32 s1, v255, 18
	s_lshl_b64 s[0:1], s[0:1], 16
	v_readlane_b32 s2, v254, 5
	s_waitcnt vmcnt(0) lgkmcnt(0)
	v_mov_b32_e32 v18, v0
	s_add_u32 s0, s2, s0
	v_readlane_b32 s2, v254, 6
	s_addc_u32 s1, s2, s1
	v_ashrrev_i32_e32 v19, 31, v18
	v_lshl_add_u64 v[28:29], v[18:19], 4, s[0:1]
	s_movk_i32 s0, 0x2000
	v_add_co_u32_e32 v6, vcc, s0, v28
	s_movk_i32 s0, 0x4000
	s_nop 0
	v_addc_co_u32_e32 v7, vcc, 0, v29, vcc
	v_add_co_u32_e32 v10, vcc, s0, v28
	s_movk_i32 s0, 0x6000
	s_nop 0
	v_addc_co_u32_e32 v11, vcc, 0, v29, vcc
	v_add_co_u32_e32 v14, vcc, s0, v28
	s_mov_b32 s0, 0x8000
	s_nop 0
	v_addc_co_u32_e32 v15, vcc, 0, v29, vcc
	v_add_co_u32_e32 v20, vcc, s0, v28
	s_mov_b32 s0, 0xa000
	s_nop 0
	v_addc_co_u32_e32 v21, vcc, 0, v29, vcc
	v_add_co_u32_e32 v24, vcc, s0, v28
	s_mov_b32 s0, 0xc000
	s_nop 0
	v_addc_co_u32_e32 v25, vcc, 0, v29, vcc
	v_add_co_u32_e32 v30, vcc, s0, v28
	s_mov_b32 s0, 0xe000
	s_nop 0
	v_addc_co_u32_e32 v31, vcc, 0, v29, vcc
	v_add_co_u32_e32 v32, vcc, s0, v28
	global_load_dwordx4 v[2:5], v[28:29], off
	s_nop 0
	global_load_dwordx4 v[6:9], v[6:7], off
	v_addc_co_u32_e32 v33, vcc, 0, v29, vcc
	global_load_dwordx4 v[10:13], v[10:11], off
	s_nop 0
	global_load_dwordx4 v[14:17], v[14:15], off
	s_nop 0
	global_load_dwordx4 v[20:23], v[20:21], off
	s_nop 0
	global_load_dwordx4 v[24:27], v[24:25], off
	s_nop 0
	global_load_dwordx4 v[28:31], v[30:31], off
	s_nop 0
	global_load_dwordx4 v[32:35], v[32:33], off
	v_readlane_b32 s0, v255, 10
	v_readlane_b32 s3, v255, 16
	v_readlane_b32 s5, v254, 60
	v_mov_b32_e32 v1, s0
	v_readlane_b32 s0, v254, 61
	s_mul_hi_u32 s1, s3, s0
	s_mul_i32 s2, s1, s5
	s_sub_i32 s2, s3, s2
	s_add_i32 s3, s1, 1
	s_sub_i32 s4, s2, s5
	s_cmp_ge_u32 s2, s5
	v_lshl_add_u32 v19, v18, 4, 0
	s_cselect_b32 s1, s3, s1
	s_cselect_b32 s2, s4, s2
	s_add_i32 s3, s1, 1
	s_cmp_ge_u32 s2, s5
	s_cselect_b32 s1, s3, s1
	v_readlane_b32 s2, v252, 10
	s_xor_b32 s1, s1, s2
	s_sub_i32 s3, s1, s2
	v_readfirstlane_b32 s0, v18
	s_cmp_lt_i32 s3, 16
	s_waitcnt vmcnt(7)
	ds_write_b128 v19, v[2:5]
	s_waitcnt vmcnt(3)
	ds_write_b128 v19, v[20:23] offset:32768
	ds_write_b128 v19, v[6:9] offset:8192
	ds_write_b128 v19, v[10:13] offset:16384
	ds_write_b128 v19, v[14:17] offset:24576
	s_waitcnt vmcnt(2)
	ds_write_b128 v19, v[24:27] offset:40960
	s_waitcnt vmcnt(1)
	ds_write_b128 v19, v[28:31] offset:49152
	s_waitcnt vmcnt(0)
	ds_write_b128 v19, v[32:35] offset:57344
	s_waitcnt lgkmcnt(0)
	s_barrier
	ds_read_b64 v[2:3], v1
	s_waitcnt lgkmcnt(0)
	v_readfirstlane_b32 s1, v2
	v_readfirstlane_b32 s2, v3
	s_cbranch_scc1 .LBB0_1214
	s_mul_i32 s4, s3, s84
	v_and_b32_e32 v26, 15, v18
	v_bfe_u32 v27, v18, 4, 2
	s_ashr_i32 s8, s0, 6
	v_lshlrev_b32_e32 v1, 3, v27
	v_add_u32_e32 v82, s4, v26
	v_lshl_or_b32 v20, s8, 7, v1
	v_ashrrev_i32_e32 v83, 31, v82
	v_readlane_b32 s10, v252, 20
	v_ashrrev_i32_e32 v21, 31, v20
	v_lshlrev_b64 v[2:3], 11, v[82:83]
	v_readlane_b32 s11, v252, 21
	v_lshlrev_b64 v[22:23], 1, v[20:21]
	s_ashr_i32 s5, s3, 31
	v_lshl_add_u64 v[2:3], s[10:11], 0, v[2:3]
	v_lshl_add_u64 v[2:3], v[2:3], 0, v[22:23]
	global_load_dwordx4 v[14:17], v[2:3], off offset:192 nt
	global_load_dwordx4 v[10:13], v[2:3], off offset:128 nt
	global_load_dwordx4 v[6:9], v[2:3], off offset:64 nt
	s_nop 0
	global_load_dwordx4 v[2:5], v[2:3], off nt
	s_lshr_b32 s5, s5, 28
	v_readlane_b32 s6, v255, 17
	s_add_i32 s3, s3, s5
	v_readlane_b32 s7, v255, 18
	s_lshl_b32 s12, s6, 10
	s_ashr_i32 s5, s3, 4
	s_lshl_b64 s[6:7], s[12:13], 2
	s_add_u32 s6, s1, s6
	s_addc_u32 s7, s2, s7
	s_add_i32 s1, 0, 0x10000
	v_lshlrev_b32_e32 v190, 2, v26
	s_andn2_b32 s0, s0, 63
	v_and_b32_e32 v18, 63, v18
	v_add_u32_e32 v1, s1, v190
	s_add_i32 s0, s0, s1
	v_lshlrev_b32_e32 v28, 8, v27
	v_readlane_b32 s1, v255, 11
	v_lshl_add_u64 v[84:85], s[10:11], 0, v[22:23]
	v_cmp_gt_u32_e64 s[36:37], 16, v18
	v_lshl_add_u32 v83, v18, 2, s0
	v_add_u32_e32 v29, s1, v190
	v_cmp_gt_u32_e64 s[38:39], 32, v18
	s_lshl_b32 s1, s8, 1
	v_readlane_b32 s2, v254, 7
	v_or_b32_e32 v18, 32, v20
	v_or_b32_e32 v22, 64, v20
	v_or_b32_e32 v24, 0x60, v20
	v_lshl_or_b32 v31, s8, 12, v28
	s_lshl_b32 s0, s8, 10
	v_add_u32_e32 v30, s1, v27
	v_readlane_b32 s3, v254, 8
	v_ashrrev_i32_e32 v19, 31, v18
	v_or_b32_e32 v92, 36, v20
	v_ashrrev_i32_e32 v23, 31, v22
	v_or_b32_e32 v94, 0x44, v20
	v_ashrrev_i32_e32 v25, 31, v24
	v_or_b32_e32 v96, 0x64, v20
	v_lshl_or_b32 v26, v26, 4, v31
	s_add_i32 s1, s1, s4
	v_lshl_add_u64 v[86:87], s[96:97], 0, v[20:21]
	v_lshl_add_u64 v[88:89], s[2:3], 0, v[190:191]
	v_lshl_add_u64 v[90:91], v[20:21], 2, s[6:7]
	v_ashrrev_i32_e32 v93, 31, v92
	v_ashrrev_i32_e32 v95, 31, v94
	v_ashrrev_i32_e32 v97, 31, v96
	v_add_u32_e32 v143, 0, v26
	v_lshl_add_u32 v156, v30, 6, v29
	v_add3_u32 v157, v29, s0, v28
	v_add_u32_e32 v158, s1, v27
	s_mov_b32 s7, 0
	v_lshlrev_b64 v[98:99], 2, v[20:21]
	v_lshlrev_b64 v[100:101], 2, v[18:19]
	v_lshlrev_b64 v[102:103], 2, v[22:23]
	v_lshlrev_b64 v[104:105], 2, v[24:25]
	s_branch .LBB0_1204

; #define GAS __attribute__((address_space(1)))
; __device__ __forceinline__ void n2_phase(const Frame& F0, int L, int nrows) {
;     ...
;         if (g + 1 < NG) {
; #pragma unroll
;             for (int s_ = 0; s_ < 4; ++s_) nraw[s_] = *(const GAS u32x4*)(X + (size_t)(row + 16) * D + c0 + 32 * s_);
;         }
.LBB0_1207:
	v_add_u32_e32 v2, 16, v140
	v_ashrrev_i32_e32 v3, 31, v2
	v_lshlrev_b64 v[2:3], 11, v[2:3]
	v_lshl_add_u64 v[14:15], v[84:85], 0, v[2:3]
	global_load_dwordx4 v[2:5], v[14:15], off nt
	global_load_dwordx4 v[6:9], v[14:15], off offset:64 nt
	global_load_dwordx4 v[10:13], v[14:15], off offset:128 nt
	s_nop 0
	global_load_dwordx4 v[14:17], v[14:15], off offset:192 nt

; #define GAS __attribute__((address_space(1)))
; #define LAS __attribute__((address_space(3)))
; #define PHASE_FRAME(F0) Frame F = F0; { int t_ = threadIdx.x; asm volatile("" : "+v"(t_)); F.tid = t_; F.lane = t_ & 63; F.wave = __builtin_amdgcn_readfirstlane(t_ >> 6); }
; __device__ __forceinline__ bf16_t* x_row_ptr(Frame& F, int row) { return (bf16_t*)(F.ws + WS_X) + (size_t)row * D; }
; #define FIN_ISSUE(R, kk) do { const int kn_ = (kk) < RPW ? (kk) : RPW - 1; rowrq_issue(F, R, rbeg + kn_, F.lane < 16 ? (unsigned)strip[kn_ * 16 + F.lane] : 0xFFFFu); } while (0)
; __device__ __forceinline__ void rowrq_issue(Frame& F, RowRq& R, int row, unsigned ts) {
;     R.row = row; R.ts = ts;
;     const GAS u32x4* xr = (const GAS u32x4*)x_row_ptr(F, row) + 2 * F.lane;
;     R.x[0] = xr[0]; R.x[1] = xr[1];
;     unsigned long long mask = __ballot(ts != 0xFFFFu);
;     unsigned vm = 0u;
; #pragma unroll
;     for (int k = 0; k < 8; ++k) {
;         const bool has = mask != 0ull;
;         const int e = has ? __builtin_ctzll(mask) : 0;
;         const unsigned sl = (unsigned)__builtin_amdgcn_readlane((int)ts, e);
;         mask &= mask - 1ull;
;         R.w[k] = *y_row_ptr16(F, row, has ? e : 0, has ? sl : 0u);
;         vm |= has ? (1u << k) : 0u;
;     }
;     R.vm = vm; R.rest = mask;
; }
; __device__ __forceinline__ void fin_phase(const Frame& F0) {
;     PHASE_FRAME(F0);
;     const int gw = blockIdx.x * 8 + F.wave, NGW = F.G * 8, RPW = NLAT / NGW, rbeg = gw * RPW;
;     LAS unsigned short* strip = (LAS unsigned short*)F.lds + F.wave * 512;
;     tokslot_preload(F, strip, rbeg, RPW);
;     LAS unsigned char* stg = F.lds + 16384 + F.wave * 5120;
;     ...
;     RowRq R0, R1, R2;
;     FIN_ISSUE(R0, 0); FIN_ISSUE(R1, 1);
.LBB0_1636:
	s_or_b64 exec, exec, s[4:5]
	s_waitcnt lgkmcnt(0)
	s_add_i32 s33, s70, -1
	s_mov_b32 s5, 0
	s_min_i32 s3, s33, 0
	v_mov_b32_e32 v135, 0xffff
	v_mov_b32_e32 v137, 0xffff
	s_and_saveexec_b64 s[6:7], s[0:1]
	s_lshl_b32 s4, s3, 5
	s_add_i32 s4, s64, s4
	v_lshl_add_u32 v0, v134, 1, s4
	ds_read_u16 v137, v0
	s_or_b64 exec, exec, s[6:7]
	s_add_i32 s6, s2, s3
	s_add_i32 s3, s6, 0xffff8000
	s_lshr_b32 s3, s3, 11
	s_waitcnt lgkmcnt(0)
	v_cmp_ne_u32_e32 vcc, v137, v135
	s_add_i32 s4, s3, 0x100
	s_ashr_i32 s7, s6, 11
	s_add_u32 s8, vcc_lo, -1
	s_addc_u32 s9, vcc_hi, -1
	s_and_b64 s[26:27], s[8:9], vcc
	s_add_u32 s8, s26, -1
	s_addc_u32 s9, s27, -1
	s_and_b64 s[24:25], s[8:9], s[26:27]
	s_add_u32 s8, s24, -1
	s_addc_u32 s9, s25, -1
	s_and_b64 s[22:23], s[8:9], s[24:25]
	s_add_u32 s8, s22, -1
	s_addc_u32 s9, s23, -1
	s_and_b64 s[20:21], s[8:9], s[22:23]
	s_add_u32 s8, s20, -1
	s_addc_u32 s9, s21, -1
	s_and_b64 s[18:19], s[8:9], s[20:21]
	s_add_u32 s8, s18, -1
	s_addc_u32 s9, s19, -1
	s_and_b64 s[8:9], s[8:9], s[18:19]
	s_cmp_eq_u64 s[8:9], 0
	s_cselect_b64 s[12:13], -1, 0
	s_ff1_i32_b64 s3, s[8:9]
	s_and_b64 s[10:11], s[12:13], exec
	s_cselect_b32 s11, 0, s3
	s_add_u32 s14, s8, -1
	s_addc_u32 s15, s9, -1
	s_lshl_b32 s3, s11, 4
	s_and_b64 s[14:15], s[14:15], s[8:9]
	s_add_i32 s28, s3, s7
	s_lshl_b32 s29, s11, 1
	s_cmp_eq_u64 s[14:15], 0
	s_cselect_b64 s[8:9], -1, 0
	s_ff1_i32_b64 s3, s[14:15]
	s_and_b64 s[16:17], s[8:9], exec
	s_cselect_b32 s3, 0, s3
	s_lshl_b32 s10, s3, 4
	s_lshl_b32 s16, s3, 1
	s_add_i32 s10, s10, s7
	s_add_i32 s16, s16, s4
	s_cmp_lt_i32 s6, 0x8000
	s_cselect_b32 s10, s10, s16
	s_add_i32 s29, s29, s4
	s_cmp_lt_i32 s6, 0x8000
	s_cselect_b32 s28, s28, s29
	s_cmp_eq_u64 s[18:19], 0
	s_cselect_b64 s[16:17], -1, 0
	s_ff1_i32_b64 s29, s[18:19]
	s_and_b64 s[18:19], s[16:17], exec
	s_cselect_b32 s29, 0, s29
	s_lshl_b32 s18, s29, 4
	s_lshl_b32 s19, s29, 1
	s_add_i32 s18, s18, s7
	s_add_i32 s19, s19, s4
	s_cmp_lt_i32 s6, 0x8000
	s_cselect_b32 s30, s18, s19
	s_cmp_eq_u64 s[20:21], 0
	s_cselect_b64 s[18:19], -1, 0
	s_ff1_i32_b64 s31, s[20:21]
	s_and_b64 s[20:21], s[18:19], exec
	s_cselect_b32 s31, 0, s31
	s_lshl_b32 s20, s31, 4
	s_lshl_b32 s21, s31, 1
	s_add_i32 s20, s20, s7
	s_add_i32 s21, s21, s4
	s_cmp_lt_i32 s6, 0x8000
	s_cselect_b32 s34, s20, s21
	s_cmp_eq_u64 s[22:23], 0
	s_cselect_b64 s[20:21], -1, 0
	s_ff1_i32_b64 s35, s[22:23]
	s_and_b64 s[22:23], s[20:21], exec
	s_cselect_b32 s35, 0, s35
	s_lshl_b32 s22, s35, 4
	s_lshl_b32 s23, s35, 1
	s_add_i32 s22, s22, s7
	s_add_i32 s23, s23, s4
	s_cmp_lt_i32 s6, 0x8000
	s_cselect_b32 s36, s22, s23
	s_cmp_eq_u64 s[24:25], 0
	s_cselect_b64 s[22:23], -1, 0
	s_ff1_i32_b64 s37, s[24:25]
	s_and_b64 s[24:25], s[22:23], exec
	s_cselect_b32 s37, 0, s37
	s_lshl_b32 s24, s37, 4
	s_lshl_b32 s25, s37, 1
	s_add_i32 s24, s24, s7
	s_add_i32 s25, s25, s4
	s_cmp_lt_i32 s6, 0x8000
	s_cselect_b32 s38, s24, s25
	s_cmp_eq_u64 s[26:27], 0
	s_cselect_b64 s[24:25], -1, 0
	s_ff1_i32_b64 s39, s[26:27]
	s_and_b64 s[26:27], s[24:25], exec
	s_cselect_b32 s39, 0, s39
	s_lshl_b32 s26, s39, 4
	s_lshl_b32 s27, s39, 1
	s_add_i32 s26, s26, s7
	s_add_i32 s27, s27, s4
	s_cmp_lt_i32 s6, 0x8000
	s_cselect_b32 s40, s26, s27
	s_cmp_lg_u64 vcc, 0
	s_cselect_b64 s[26:27], -1, 0
	s_ff1_i32_b64 s41, vcc
	s_and_b64 s[42:43], s[26:27], exec
	s_cselect_b32 s41, s41, 0
	s_lshl_b32 s42, s41, 4
	s_add_i32 s42, s42, s7
	s_lshl_b32 s7, s41, 1
	s_add_i32 s7, s7, s4
	s_cmp_lt_i32 s6, 0x8000
	s_cselect_b32 s42, s42, s7
	s_ashr_i32 s7, s6, 31
	s_lshl_b64 s[46:47], s[6:7], 11
	s_add_u32 s46, s68, s46
	s_addc_u32 s47, s69, s47
	v_lshlrev_b32_e32 v0, 5, v134
	v_readlane_b32 s4, v137, s41
	s_ashr_i32 s43, s42, 31
	global_load_dwordx4 v[72:75], v0, s[46:47] offset:16 nt
	global_load_dwordx4 v[76:79], v0, s[46:47] nt
	s_lshl_b64 s[42:43], s[42:43], 18
	s_lshl_b64 s[46:47], s[4:5], 10
	s_and_b64 s[48:49], s[26:27], exec
	s_cselect_b32 s4, s47, 0
	s_cselect_b32 s7, s46, 0
	s_add_u32 s41, s90, s42
	s_addc_u32 s43, s91, s43
	s_add_u32 s42, s41, s7
	s_addc_u32 s43, s43, s4
	v_readlane_b32 s4, v137, s39
	s_ashr_i32 s41, s40, 31
	s_lshl_b64 s[40:41], s[40:41], 18
	s_lshl_b64 s[46:47], s[4:5], 10
	s_and_b64 s[48:49], s[24:25], exec
	s_cselect_b32 s4, 0, s47
	s_cselect_b32 s7, 0, s46
	s_add_u32 s39, s90, s40
	s_addc_u32 s41, s91, s41
	s_add_u32 s40, s39, s7
	v_lshlrev_b32_e32 v128, 4, v134
	s_addc_u32 s41, s41, s4
	v_readlane_b32 s4, v137, s37
	s_ashr_i32 s39, s38, 31
	global_load_dwordx4 v[68:71], v128, s[42:43]
	global_load_dwordx4 v[64:67], v128, s[40:41]
	s_lshl_b64 s[38:39], s[38:39], 18
	s_lshl_b64 s[40:41], s[4:5], 10
	s_and_b64 s[42:43], s[22:23], exec
	s_cselect_b32 s4, 0, s41
	s_cselect_b32 s7, 0, s40
	s_add_u32 s37, s90, s38
	s_addc_u32 s39, s91, s39
	s_add_u32 s38, s37, s7
	s_addc_u32 s39, s39, s4
	v_readlane_b32 s4, v137, s35
	s_ashr_i32 s37, s36, 31
	s_lshl_b64 s[36:37], s[36:37], 18
	s_lshl_b64 s[40:41], s[4:5], 10
	s_and_b64 s[42:43], s[20:21], exec
	s_cselect_b32 s4, 0, s41
	s_cselect_b32 s7, 0, s40
	s_add_u32 s35, s90, s36
	s_addc_u32 s37, s91, s37
	s_add_u32 s36, s35, s7
	s_addc_u32 s37, s37, s4
	v_readlane_b32 s4, v137, s31
	s_ashr_i32 s35, s34, 31
	global_load_dwordx4 v[60:63], v128, s[38:39]
	global_load_dwordx4 v[48:51], v128, s[36:37]
	s_lshl_b64 s[34:35], s[34:35], 18
	s_lshl_b64 s[36:37], s[4:5], 10
	s_and_b64 s[38:39], s[18:19], exec
	s_cselect_b32 s4, 0, s37
	s_cselect_b32 s7, 0, s36
	s_add_u32 s31, s90, s34
	s_addc_u32 s35, s91, s35
	s_add_u32 s34, s31, s7
	s_addc_u32 s35, s35, s4
	v_readlane_b32 s4, v137, s29
	s_ashr_i32 s31, s30, 31
	s_lshl_b64 s[30:31], s[30:31], 18
	s_lshl_b64 s[36:37], s[4:5], 10
	s_and_b64 s[38:39], s[16:17], exec
	s_cselect_b32 s4, 0, s37
	s_cselect_b32 s7, 0, s36
	s_add_u32 s29, s90, s30
	s_addc_u32 s31, s91, s31
	s_add_u32 s30, s29, s7
	s_addc_u32 s31, s31, s4
	v_readlane_b32 s4, v137, s11
	s_ashr_i32 s29, s28, 31
	global_load_dwordx4 v[40:43], v128, s[34:35]
	global_load_dwordx4 v[32:35], v128, s[30:31]
	s_lshl_b64 s[28:29], s[28:29], 18
	s_lshl_b64 s[30:31], s[4:5], 10
	s_and_b64 s[34:35], s[12:13], exec
	s_cselect_b32 s4, 0, s31
	s_cselect_b32 s7, 0, s30
	s_add_u32 s11, s90, s28
	s_addc_u32 s29, s91, s29
	s_add_u32 s28, s11, s7
	s_addc_u32 s29, s29, s4
	v_readlane_b32 s4, v137, s3
	s_ashr_i32 s11, s10, 31
	s_lshl_b64 s[10:11], s[10:11], 18
	s_lshl_b64 s[4:5], s[4:5], 10
	s_and_b64 s[30:31], s[8:9], exec
	s_cselect_b32 s3, 0, s5
	s_cselect_b32 s4, 0, s4
	s_add_u32 s5, s90, s10
	s_addc_u32 s7, s91, s11
	s_add_u32 s4, s5, s4
	s_addc_u32 s5, s7, s3
	global_load_dwordx4 v[24:27], v128, s[28:29]
	global_load_dwordx4 v[16:19], v128, s[4:5]
	v_lshlrev_b32_e32 v0, 1, v134
	s_min_i32 s3, s33, 1
	s_and_saveexec_b64 s[4:5], s[0:1]
	s_lshl_b32 s7, s3, 5
	s_add_i32 s7, s64, s7
	v_lshl_add_u32 v1, v134, 1, s7
	ds_read_u16 v135, v1
	s_or_b64 exec, exec, s[4:5]
	s_add_i32 s4, s2, s3
	s_add_i32 s3, s4, 0xffff8000
	s_mov_b32 s86, 0xffff
	s_lshr_b32 s3, s3, 11
	s_waitcnt lgkmcnt(0)
; #define GAS __attribute__((address_space(1)))
; __device__ __forceinline__ bf16_t* x_row_ptr(Frame& F, int row) { return (bf16_t*)(F.ws + WS_X) + (size_t)row * D; }
; __device__ __forceinline__ void rowrq_issue(Frame& F, RowRq& R, int row, unsigned ts) {
;     R.row = row; R.ts = ts;
;     const GAS u32x4* xr = (const GAS u32x4*)x_row_ptr(F, row) + 2 * F.lane;
;     R.x[0] = xr[0]; R.x[1] = xr[1];
;     unsigned long long mask = __ballot(ts != 0xFFFFu);
;     unsigned vm = 0u;
; #pragma unroll
;     for (int k = 0; k < 8; ++k) {
;         const bool has = mask != 0ull;
;         const int e = has ? __builtin_ctzll(mask) : 0;
;         const unsigned sl = (unsigned)__builtin_amdgcn_readlane((int)ts, e);
;         mask &= mask - 1ull;
;         R.w[k] = *y_row_ptr16(F, row, has ? e : 0, has ? sl : 0u);
;         vm |= has ? (1u << k) : 0u;
;     }
;     R.vm = vm; R.rest = mask;
; }
	v_cmp_ne_u32_e32 vcc, s86, v135
	s_addk_i32 s3, 0x100
	s_ashr_i32 s5, s4, 11
	s_add_u32 s10, vcc_lo, -1
	s_addc_u32 s11, vcc_hi, -1
	s_and_b64 s[38:39], s[10:11], vcc
	s_add_u32 s10, s38, -1
	s_addc_u32 s11, s39, -1
	s_and_b64 s[50:51], s[10:11], s[38:39]
	s_add_u32 s10, s50, -1
	s_addc_u32 s11, s51, -1
	s_and_b64 s[48:49], s[10:11], s[50:51]
	s_add_u32 s10, s48, -1
	s_addc_u32 s11, s49, -1
	s_and_b64 s[46:47], s[10:11], s[48:49]
	s_add_u32 s10, s46, -1
	s_addc_u32 s11, s47, -1
	s_and_b64 s[42:43], s[10:11], s[46:47]
	s_add_u32 s10, s42, -1
	s_addc_u32 s11, s43, -1
	s_and_b64 s[28:29], s[10:11], s[42:43]
	s_cmp_eq_u64 s[28:29], 0
	s_cselect_b64 s[34:35], -1, 0
	s_ff1_i32_b64 s7, s[28:29]
	s_and_b64 s[30:31], s[34:35], exec
	s_cselect_b32 s31, 0, s7
	s_add_u32 s36, s28, -1
	s_addc_u32 s37, s29, -1
	s_lshl_b32 s7, s31, 4
	s_and_b64 s[36:37], s[36:37], s[28:29]
	s_add_i32 s7, s7, s5
	s_lshl_b32 s10, s31, 1
	s_cmp_eq_u64 s[36:37], 0
	s_cselect_b64 s[28:29], -1, 0
	s_ff1_i32_b64 s30, s[36:37]
	s_and_b64 s[40:41], s[28:29], exec
	s_cselect_b32 s65, 0, s30
	s_lshl_b32 s30, s65, 4
	s_lshl_b32 s40, s65, 1
	s_add_i32 s30, s30, s5
	s_add_i32 s40, s40, s3
	s_cmp_lt_i32 s4, 0x8000
	s_cselect_b32 s30, s30, s40
	s_add_i32 s10, s10, s3
	s_cmp_lt_i32 s4, 0x8000
	s_cselect_b32 s44, s7, s10
	s_cmp_eq_u64 s[42:43], 0
	s_cselect_b64 s[40:41], -1, 0
	s_ff1_i32_b64 s7, s[42:43]
	s_and_b64 s[42:43], s[40:41], exec
	s_cselect_b32 s53, 0, s7
	s_lshl_b32 s7, s53, 4
	s_lshl_b32 s10, s53, 1
	s_add_i32 s7, s7, s5
	s_add_i32 s10, s10, s3
	s_cmp_lt_i32 s4, 0x8000
	s_cselect_b32 s52, s7, s10
	s_cmp_eq_u64 s[46:47], 0
	s_cselect_b64 s[42:43], -1, 0
	s_ff1_i32_b64 s7, s[46:47]
	s_and_b64 s[46:47], s[42:43], exec
	s_cselect_b32 s55, 0, s7
	s_lshl_b32 s7, s55, 4
	s_lshl_b32 s10, s55, 1
	s_add_i32 s7, s7, s5
	s_add_i32 s10, s10, s3
	s_cmp_lt_i32 s4, 0x8000
	s_cselect_b32 s54, s7, s10
	s_cmp_eq_u64 s[48:49], 0
	s_cselect_b64 s[46:47], -1, 0
	s_ff1_i32_b64 s7, s[48:49]
	s_and_b64 s[48:49], s[46:47], exec
	s_cselect_b32 s57, 0, s7
	s_lshl_b32 s7, s57, 4
	s_lshl_b32 s10, s57, 1
	s_add_i32 s7, s7, s5
	s_add_i32 s10, s10, s3
	s_cmp_lt_i32 s4, 0x8000
	s_cselect_b32 s56, s7, s10
	s_cmp_eq_u64 s[50:51], 0
	s_cselect_b64 s[48:49], -1, 0
	s_ff1_i32_b64 s7, s[50:51]
	s_and_b64 s[50:51], s[48:49], exec
	s_cselect_b32 s59, 0, s7
	s_lshl_b32 s7, s59, 4
	s_lshl_b32 s10, s59, 1
	s_add_i32 s7, s7, s5
	s_add_i32 s10, s10, s3
	s_cmp_lt_i32 s4, 0x8000
	s_cselect_b32 s58, s7, s10
	s_cmp_eq_u64 s[38:39], 0
	s_cselect_b64 s[50:51], -1, 0
	s_ff1_i32_b64 s7, s[38:39]
	s_and_b64 s[38:39], s[50:51], exec
	s_cselect_b32 s61, 0, s7
	s_lshl_b32 s7, s61, 4
	s_lshl_b32 s10, s61, 1
	s_add_i32 s7, s7, s5
	s_add_i32 s10, s10, s3
	s_cmp_lt_i32 s4, 0x8000
	s_cselect_b32 s60, s7, s10
	s_cmp_lg_u64 vcc, 0
	s_cselect_b64 s[62:63], -1, 0
	s_ff1_i32_b64 s7, vcc
	s_and_b64 s[38:39], s[62:63], exec
	s_cselect_b32 s10, s7, 0
	s_lshl_b32 s7, s10, 4
	s_add_i32 s7, s7, s5
	s_lshl_b32 s5, s10, 1
	s_add_i32 s5, s5, s3
	s_cmp_lt_i32 s4, 0x8000
	s_cselect_b32 s66, s7, s5
	s_add_u32 s38, s14, -1
	s_addc_u32 s39, s15, -1
	s_and_b64 s[38:39], s[38:39], s[14:15]
	s_and_b64 s[12:13], s[12:13], exec
	s_cselect_b32 s3, 0, 64
	s_and_b64 s[12:13], s[16:17], exec
	s_cselect_b32 s5, 0, 32
	s_and_b64 s[12:13], s[18:19], exec
	s_cselect_b32 s7, 0, 16
	s_and_b64 s[12:13], s[20:21], exec
	s_cselect_b32 s14, 0, 8
	s_and_b64 s[12:13], s[22:23], exec
	s_waitcnt vmcnt(0)
; #define GAS __attribute__((address_space(1)))
; #define LAS __attribute__((address_space(3)))
; __device__ __forceinline__ bf16_t* x_row_ptr(Frame& F, int row) { return (bf16_t*)(F.ws + WS_X) + (size_t)row * D; }
; #define FIN_ISSUE(R, kk) do { const int kn_ = (kk) < RPW ? (kk) : RPW - 1; rowrq_issue(F, R, rbeg + kn_, F.lane < 16 ? (unsigned)strip[kn_ * 16 + F.lane] : 0xFFFFu); } while (0)
; __device__ __forceinline__ void rowrq_issue(Frame& F, RowRq& R, int row, unsigned ts) {
;     R.row = row; R.ts = ts;
;     const GAS u32x4* xr = (const GAS u32x4*)x_row_ptr(F, row) + 2 * F.lane;
;     R.x[0] = xr[0]; R.x[1] = xr[1];
;     unsigned long long mask = __ballot(ts != 0xFFFFu);
;     unsigned vm = 0u;
; #pragma unroll
;     for (int k = 0; k < 8; ++k) {
;         const bool has = mask != 0ull;
;         const int e = has ? __builtin_ctzll(mask) : 0;
;         const unsigned sl = (unsigned)__builtin_amdgcn_readlane((int)ts, e);
;         mask &= mask - 1ull;
;         R.w[k] = *y_row_ptr16(F, row, has ? e : 0, has ? sl : 0u);
;         vm |= has ? (1u << k) : 0u;
;     }
;     R.vm = vm; R.rest = mask;
; }
; __device__ __forceinline__ void fin_phase(const Frame& F0) {
;     ...
;     LAS unsigned char* stg = F.lds + 16384 + F.wave * 5120;
;     ...
;     RowRq R0, R1, R2;
;     FIN_ISSUE(R0, 0); FIN_ISSUE(R1, 1);
;     int k = 0;
;     for (; k + 2 < RPW; k += 3) { FIN_STEP(R0, R2, k); FIN_STEP(R1, R0, k + 1); FIN_STEP(R2, R1, k + 2); }
	v_cndmask_b32_e64 v2, 0, 1, s[26:27]
	s_cselect_b32 s15, 0, 4
	s_and_b64 s[12:13], s[24:25], exec
	s_cselect_b32 s12, 0, 2
	v_readfirstlane_b32 s13, v2
	s_or_b32 s12, s12, s13
	s_or_b32 s12, s12, s15
	s_or_b32 s12, s12, s14
	s_or_b32 s7, s12, s7
	s_or_b32 s5, s7, s5
	s_or_b32 s3, s5, s3
	s_and_b64 s[8:9], s[8:9], exec
	s_cselect_b32 s5, 0, 0x80
	s_or_b32 s7, s3, s5
	s_lshl_b32 s3, s45, 12
	s_ashr_i32 s5, s4, 31
	s_add_i32 s20, s64, s3
	s_lshl_b64 s[8:9], s[4:5], 11
	s_add_u32 s8, s68, s8
	s_mov_b32 s11, 0
	s_addc_u32 s9, s69, s9
	v_lshlrev_b32_e32 v80, 4, v0
	v_readlane_b32 s10, v135, s10
	s_ashr_i32 s67, s66, 31
	global_load_dwordx4 v[52:55], v80, s[8:9] offset:16 nt
	global_load_dwordx4 v[56:59], v80, s[8:9] nt
	s_lshl_b64 s[8:9], s[66:67], 18
	s_lshl_b64 s[12:13], s[10:11], 10
	s_and_b64 s[14:15], s[62:63], exec
	s_cselect_b32 s3, s13, 0
	s_cselect_b32 s5, s12, 0
	s_add_u32 s8, s90, s8
	s_addc_u32 s9, s91, s9
	s_add_u32 s8, s8, s5
	s_addc_u32 s9, s9, s3
	v_readlane_b32 s10, v135, s61
	s_ashr_i32 s61, s60, 31
	s_lshl_b64 s[12:13], s[60:61], 18
	s_lshl_b64 s[14:15], s[10:11], 10
	s_and_b64 s[16:17], s[50:51], exec
	s_cselect_b32 s3, 0, s15
	s_cselect_b32 s5, 0, s14
	s_add_u32 s10, s90, s12
	s_addc_u32 s13, s91, s13
	s_add_u32 s12, s10, s5
	s_addc_u32 s13, s13, s3
	v_readlane_b32 s10, v135, s59
	s_ashr_i32 s59, s58, 31
	global_load_dwordx4 v[44:47], v128, s[8:9]
	global_load_dwordx4 v[36:39], v128, s[12:13]
	s_lshl_b64 s[8:9], s[58:59], 18
	s_lshl_b64 s[12:13], s[10:11], 10
	s_and_b64 s[14:15], s[48:49], exec
	s_cselect_b32 s3, 0, s13
	s_cselect_b32 s5, 0, s12
	s_add_u32 s8, s90, s8
	s_addc_u32 s9, s91, s9
	s_add_u32 s8, s8, s5
	s_addc_u32 s9, s9, s3
	v_readlane_b32 s10, v135, s57
	s_ashr_i32 s57, s56, 31
	s_lshl_b64 s[12:13], s[56:57], 18
	s_lshl_b64 s[14:15], s[10:11], 10
	s_and_b64 s[16:17], s[46:47], exec
	s_cselect_b32 s3, 0, s15
	s_cselect_b32 s5, 0, s14
	s_add_u32 s10, s90, s12
	s_addc_u32 s13, s91, s13
	s_add_u32 s12, s10, s5
	s_addc_u32 s13, s13, s3
	v_readlane_b32 s10, v135, s55
	s_ashr_i32 s55, s54, 31
	global_load_dwordx4 v[28:31], v128, s[8:9]
	global_load_dwordx4 v[20:23], v128, s[12:13]
	s_lshl_b64 s[8:9], s[54:55], 18
	s_lshl_b64 s[12:13], s[10:11], 10
	s_and_b64 s[14:15], s[42:43], exec
	s_cselect_b32 s3, 0, s13
	s_cselect_b32 s5, 0, s12
	s_add_u32 s8, s90, s8
	s_addc_u32 s9, s91, s9
	s_add_u32 s8, s8, s5
	s_addc_u32 s9, s9, s3
	v_readlane_b32 s10, v135, s53
	s_ashr_i32 s53, s52, 31
	s_lshl_b64 s[12:13], s[52:53], 18
	s_lshl_b64 s[14:15], s[10:11], 10
	s_and_b64 s[16:17], s[40:41], exec
	s_cselect_b32 s3, 0, s15
	s_cselect_b32 s5, 0, s14
	s_add_u32 s10, s90, s12
	s_addc_u32 s13, s91, s13
	s_add_u32 s12, s10, s5
	s_addc_u32 s13, s13, s3
	v_readlane_b32 s10, v135, s31
	s_ashr_i32 s45, s44, 31
	global_load_dwordx4 v[12:15], v128, s[8:9]
	global_load_dwordx4 v[8:11], v128, s[12:13]
	s_lshl_b64 s[8:9], s[44:45], 18
	s_lshl_b64 s[12:13], s[10:11], 10
	s_and_b64 s[14:15], s[34:35], exec
	s_cselect_b32 s3, 0, s13
	s_cselect_b32 s5, 0, s12
	s_add_u32 s8, s90, s8
	s_addc_u32 s9, s91, s9
	s_add_u32 s12, s8, s5
	s_addc_u32 s13, s9, s3
	s_add_u32 s8, s36, -1
	s_addc_u32 s9, s37, -1
	s_and_b64 s[8:9], s[8:9], s[36:37]
	s_and_b64 s[14:15], s[34:35], exec
	s_cselect_b32 s3, 0, 64
	s_and_b64 s[14:15], s[40:41], exec
	s_cselect_b32 s5, 0, 32
	s_and_b64 s[14:15], s[42:43], exec
	s_cselect_b32 s16, 0, 16
	s_and_b64 s[14:15], s[46:47], exec
	s_cselect_b32 s17, 0, 8
	s_and_b64 s[14:15], s[48:49], exec
	v_cndmask_b32_e64 v1, 0, 1, s[62:63]
	s_cselect_b32 s18, 0, 4
	s_and_b64 s[14:15], s[50:51], exec
	s_cselect_b32 s14, 0, 2
	v_readfirstlane_b32 s15, v1
	s_or_b32 s14, s14, s15
	s_or_b32 s14, s14, s18
	s_or_b32 s14, s14, s17
	s_or_b32 s14, s14, s16
	v_readlane_b32 s10, v135, s65
	s_or_b32 s5, s14, s5
	s_ashr_i32 s31, s30, 31
	s_or_b32 s3, s5, s3
	s_lshl_b64 s[14:15], s[30:31], 18
	s_lshl_b64 s[16:17], s[10:11], 10
	s_and_b64 s[18:19], s[28:29], exec
	s_cselect_b32 s5, 0, s17
	s_cselect_b32 s10, 0, s16
	s_add_u32 s14, s90, s14
	s_addc_u32 s15, s91, s15
	s_add_u32 s14, s14, s10
	s_addc_u32 s15, s15, s5
	global_load_dwordx4 v[4:7], v128, s[12:13]
	global_load_dwordx4 v[0:3], v128, s[14:15]
	s_and_b64 s[12:13], s[28:29], exec
	s_cselect_b32 s5, 0, 0x80
	s_or_b32 s5, s3, s5
	s_cmp_lt_i32 s70, 3
	v_lshrrev_b32_e32 v136, 2, v134
	v_or_b32_e32 v138, 64, v134
	s_cbranch_scc1 .LBB0_1706
	v_and_b32_e32 v81, 48, v128
	v_add_u32_e32 v83, s20, v81
	v_lshrrev_b32_e32 v81, 2, v138
	v_mul_u32_u24_e32 v85, 0x50, v81
	v_or_b32_e32 v81, 0x80, v134
	v_lshrrev_b32_e32 v81, 2, v81
	v_mul_u32_u24_e32 v86, 0x50, v81
	v_or_b32_e32 v81, 0xc0, v134
	v_lshrrev_b32_e32 v81, 2, v81
	v_mul_u32_u24_e32 v87, 0x50, v81
	v_mov_b32_e32 v81, 0
	v_mul_u32_u24_e32 v82, 0x50, v134
	v_mul_u32_u24_e32 v84, 0x50, v136
	v_writelane_b32 v252, s70, 11
	v_mov_b32_e32 v129, v81
	v_lshl_add_u32 v139, v134, 1, s64
	s_add_i32 s3, s70, -5
	v_lshl_add_u64 v[130:131], s[68:69], 0, v[80:81]
	v_lshl_add_u64 v[132:133], s[80:81], 0, v[128:129]
	s_mov_b32 s13, 0
	s_mov_b32 s10, 0x3c800000
	v_writelane_b32 v252, s20, 13
	v_add_u32_e32 v129, s20, v82
	v_add_u32_e32 v140, v83, v84
	v_add_u32_e32 v141, v83, v85
	v_add_u32_e32 v142, v83, v86
	v_add_u32_e32 v143, v83, v87
	s_mov_b32 s87, 0
	s_add_i32 s11, s87, 2
	v_mov_b32_e32 v144, 0xffff
	s_and_saveexec_b64 s[14:15], s[0:1]
	s_branch .LBB0_1643

; #define GAS __attribute__((address_space(1)))
; __device__ __forceinline__ bf16_t* x_row_ptr(Frame& F, int row) { return (bf16_t*)(F.ws + WS_X) + (size_t)row * D; }
; __device__ __forceinline__ void rowrq_issue(Frame& F, RowRq& R, int row, unsigned ts) {
;     R.row = row; R.ts = ts;
;     const GAS u32x4* xr = (const GAS u32x4*)x_row_ptr(F, row) + 2 * F.lane;
;     R.x[0] = xr[0]; R.x[1] = xr[1];
;     unsigned long long mask = __ballot(ts != 0xFFFFu);
;     unsigned vm = 0u;
; #pragma unroll
;     for (int k = 0; k < 8; ++k) {
;         const bool has = mask != 0ull;
;         const int e = has ? __builtin_ctzll(mask) : 0;
;         const unsigned sl = (unsigned)__builtin_amdgcn_readlane((int)ts, e);
;         mask &= mask - 1ull;
;         R.w[k] = *y_row_ptr16(F, row, has ? e : 0, has ? sl : 0u);
;         vm |= has ? (1u << k) : 0u;
;     }
;     R.vm = vm; R.rest = mask;
; }
.LBB0_1643:
	v_lshl_add_u32 v80, s11, 5, v139
	ds_read_u16 v144, v80
	s_or_b64 exec, exec, s[14:15]
	s_add_i32 s14, s11, s2
	s_add_i32 s11, s14, 0xffff8000
	s_lshr_b32 s88, s11, 11
	s_waitcnt lgkmcnt(0)
	v_cmp_ne_u32_e32 vcc, s86, v144
	s_addk_i32 s88, 0x100
	s_ashr_i32 s89, s14, 11
	s_add_u32 s16, vcc_lo, -1
	s_addc_u32 s17, vcc_hi, -1
	s_and_b64 s[34:35], s[16:17], vcc
	s_add_u32 s16, s34, -1
	s_addc_u32 s17, s35, -1
	s_and_b64 s[30:31], s[16:17], s[34:35]
	s_add_u32 s16, s30, -1
	s_addc_u32 s17, s31, -1
	s_and_b64 s[28:29], s[16:17], s[30:31]
	s_add_u32 s16, s28, -1
	s_addc_u32 s17, s29, -1
	s_and_b64 s[26:27], s[16:17], s[28:29]
	s_add_u32 s16, s26, -1
	s_addc_u32 s17, s27, -1
	s_and_b64 s[24:25], s[16:17], s[26:27]
	s_add_u32 s16, s24, -1
	s_addc_u32 s17, s25, -1
	s_and_b64 s[22:23], s[16:17], s[24:25]
	s_cmp_eq_u64 s[22:23], 0
	s_cselect_b64 s[20:21], -1, 0
	s_ff1_i32_b64 s11, s[22:23]
	s_and_b64 s[16:17], s[20:21], exec
	s_cselect_b32 s43, 0, s11
	s_add_u32 s16, s22, -1
	s_addc_u32 s17, s23, -1
	s_lshl_b32 s11, s43, 4
	s_and_b64 s[18:19], s[16:17], s[22:23]
	s_add_i32 s12, s11, s89
	s_lshl_b32 s15, s43, 1
	s_cmp_eq_u64 s[18:19], 0
	s_cselect_b64 s[40:41], -1, 0
	s_ff1_i32_b64 s11, s[18:19]
	s_and_b64 s[16:17], s[40:41], exec
	s_cselect_b32 s11, 0, s11
	s_lshl_b32 s16, s11, 4
	s_add_i32 s36, s16, s89
	s_lshl_b32 s16, s11, 1
	s_add_i32 s37, s16, s88
	s_cmp_lt_i32 s14, 0x8000
	s_cselect_b64 s[16:17], -1, 0
	s_and_b64 s[16:17], s[16:17], exec
	s_cselect_b32 s42, s36, s37
	s_add_i32 s15, s15, s88
	s_cmp_lt_i32 s14, 0x8000
	s_cselect_b64 s[16:17], -1, 0
	s_and_b64 s[16:17], s[16:17], exec
	s_cselect_b32 s44, s12, s15
	s_cmp_eq_u64 s[24:25], 0
	s_cselect_b64 s[46:47], -1, 0
	s_ff1_i32_b64 s12, s[24:25]
	s_and_b64 s[16:17], s[46:47], exec
	s_cselect_b32 s45, 0, s12
	s_lshl_b32 s12, s45, 4
	s_lshl_b32 s15, s45, 1
	s_add_i32 s12, s12, s89
	s_add_i32 s15, s15, s88
	s_cmp_lt_i32 s14, 0x8000
	s_cselect_b64 s[16:17], -1, 0
	s_and_b64 s[16:17], s[16:17], exec
	s_cselect_b32 s48, s12, s15
	s_cmp_eq_u64 s[26:27], 0
	s_cselect_b64 s[50:51], -1, 0
	s_ff1_i32_b64 s12, s[26:27]
	s_and_b64 s[16:17], s[50:51], exec
	s_cselect_b32 s49, 0, s12
	s_lshl_b32 s12, s49, 4
	s_lshl_b32 s15, s49, 1
	s_add_i32 s12, s12, s89
	s_add_i32 s15, s15, s88
	s_cmp_lt_i32 s14, 0x8000
	s_cselect_b64 s[16:17], -1, 0
	s_and_b64 s[16:17], s[16:17], exec
	s_cselect_b32 s52, s12, s15
	s_cmp_eq_u64 s[28:29], 0
	s_cselect_b64 s[54:55], -1, 0
	s_ff1_i32_b64 s12, s[28:29]
	s_and_b64 s[16:17], s[54:55], exec
	s_cselect_b32 s53, 0, s12
	s_lshl_b32 s12, s53, 4
	s_lshl_b32 s15, s53, 1
	s_add_i32 s12, s12, s89
	s_add_i32 s15, s15, s88
	s_cmp_lt_i32 s14, 0x8000
	s_cselect_b64 s[16:17], -1, 0
	s_and_b64 s[16:17], s[16:17], exec
	s_cselect_b32 s56, s12, s15
	s_cmp_eq_u64 s[30:31], 0
	s_cselect_b64 s[58:59], -1, 0
	s_ff1_i32_b64 s12, s[30:31]
	s_and_b64 s[16:17], s[58:59], exec
	s_cselect_b32 s57, 0, s12
	s_lshl_b32 s12, s57, 4
	s_lshl_b32 s15, s57, 1
	s_add_i32 s12, s12, s89
	s_add_i32 s15, s15, s88
	s_cmp_lt_i32 s14, 0x8000
	s_cselect_b64 s[16:17], -1, 0
	s_and_b64 s[16:17], s[16:17], exec
	s_cselect_b32 s60, s12, s15
	s_cmp_eq_u64 s[34:35], 0
	s_cselect_b64 s[62:63], -1, 0
	s_ff1_i32_b64 s12, s[34:35]
	s_and_b64 s[16:17], s[62:63], exec
	s_cselect_b32 s61, 0, s12
	s_lshl_b32 s12, s61, 4
	s_lshl_b32 s15, s61, 1
	s_add_i32 s12, s12, s89
	s_add_i32 s15, s15, s88
	s_cmp_lt_i32 s14, 0x8000
	s_cselect_b64 s[16:17], -1, 0
	s_and_b64 s[16:17], s[16:17], exec
	s_cselect_b32 s64, s12, s15
	s_cmp_eq_u64 vcc, 0
	s_cselect_b64 s[66:67], -1, 0
	s_ff1_i32_b64 s12, vcc
	s_and_b64 s[16:17], s[66:67], exec
	s_cselect_b32 s12, 0, s12
	s_lshl_b32 s15, s12, 4
	s_lshl_b32 s16, s12, 1
	s_add_i32 s15, s15, s89
	s_add_i32 s65, s16, s88
	s_cmp_lt_i32 s14, 0x8000
	s_cselect_b64 s[16:17], -1, 0
	s_and_b64 s[36:37], s[16:17], exec
	s_cselect_b32 s68, s15, s65
	s_ashr_i32 s15, s14, 31
	s_lshl_b64 s[36:37], s[14:15], 11
	s_cmp_lg_u64 vcc, 0
	v_lshl_add_u64 v[80:81], v[130:131], 0, s[36:37]
	s_cselect_b64 s[36:37], -1, 0
	v_readlane_b32 s12, v144, s12
	s_ashr_i32 s69, s68, 31
	s_lshl_b64 s[68:69], s[68:69], 18
	s_lshl_b64 s[70:71], s[12:13], 10
	s_and_b64 s[66:67], s[66:67], exec
	s_cselect_b32 s12, 0, s71
	s_cselect_b32 s65, 0, s70
	s_add_u32 s66, s90, s68
	s_addc_u32 s67, s91, s69
	s_add_u32 s66, s66, s65
	s_addc_u32 s67, s67, s12
	s_cmp_lg_u64 s[34:35], 0
	s_cselect_b64 s[34:35], -1, 0
	v_readlane_b32 s12, v144, s61
	s_ashr_i32 s65, s64, 31
	s_lshl_b64 s[64:65], s[64:65], 18
	s_lshl_b64 s[68:69], s[12:13], 10
	s_and_b64 s[62:63], s[62:63], exec
	s_cselect_b32 s12, 0, s69
	s_cselect_b32 s61, 0, s68
	s_add_u32 s62, s90, s64
	s_addc_u32 s63, s91, s65
	s_add_u32 s62, s62, s61
; #define GAS __attribute__((address_space(1)))
; __device__ __forceinline__ bf16_t* x_row_ptr(Frame& F, int row) { return (bf16_t*)(F.ws + WS_X) + (size_t)row * D; }
; __device__ __forceinline__ void rowrq_issue(Frame& F, RowRq& R, int row, unsigned ts) {
;     R.row = row; R.ts = ts;
;     const GAS u32x4* xr = (const GAS u32x4*)x_row_ptr(F, row) + 2 * F.lane;
;     R.x[0] = xr[0]; R.x[1] = xr[1];
;     unsigned long long mask = __ballot(ts != 0xFFFFu);
;     unsigned vm = 0u;
; #pragma unroll
;     for (int k = 0; k < 8; ++k) {
;         const bool has = mask != 0ull;
;         const int e = has ? __builtin_ctzll(mask) : 0;
;         const unsigned sl = (unsigned)__builtin_amdgcn_readlane((int)ts, e);
;         mask &= mask - 1ull;
;         R.w[k] = *y_row_ptr16(F, row, has ? e : 0, has ? sl : 0u);
;         vm |= has ? (1u << k) : 0u;
;     }
;     R.vm = vm; R.rest = mask;
; }
; __device__ __forceinline__ void rowrq_consume(Frame& F, const RowRq& R, f32x4 (&v)[4]) {
; #pragma unroll
;     for (int h = 0; h < 2; ++h) { const u32x4 x = R.x[h]; v[2 * h] = (f32x4){bf_lo(x.x), bf_hi(x.x), bf_lo(x.y), bf_hi(x.y)}; v[2 * h + 1] = (f32x4){bf_lo(x.z), bf_hi(x.z), bf_lo(x.w), bf_hi(x.w)}; }
; #pragma unroll
;     for (int k = 0; k < 8; ++k)
;         if ((R.vm >> k) & 1u) {
; #pragma unroll
;             for (int q = 0; q < 4; ++q) y_add4(v[q], R.w[k][q]); }
	s_addc_u32 s63, s63, s12
	s_cmp_lg_u64 s[30:31], 0
	s_cselect_b64 s[30:31], -1, 0
	v_readlane_b32 s12, v144, s57
	s_ashr_i32 s61, s60, 31
	global_load_dwordx4 v[112:115], v[80:81], off offset:16 nt
	global_load_dwordx4 v[116:119], v[80:81], off nt
	global_load_dwordx4 v[108:111], v128, s[66:67]
	global_load_dwordx4 v[104:107], v128, s[62:63]
	s_lshl_b64 s[60:61], s[60:61], 18
	s_lshl_b64 s[62:63], s[12:13], 10
	s_and_b64 s[58:59], s[58:59], exec
	s_cselect_b32 s12, 0, s63
	s_cselect_b32 s57, 0, s62
	s_add_u32 s58, s90, s60
	s_addc_u32 s59, s91, s61
	s_add_u32 s58, s58, s57
	s_addc_u32 s59, s59, s12
	s_cmp_lg_u64 s[28:29], 0
	s_cselect_b64 s[28:29], -1, 0
	v_readlane_b32 s12, v144, s53
	s_ashr_i32 s57, s56, 31
	s_lshl_b64 s[56:57], s[56:57], 18
	s_lshl_b64 s[60:61], s[12:13], 10
	s_and_b64 s[54:55], s[54:55], exec
	s_cselect_b32 s12, 0, s61
	s_cselect_b32 s53, 0, s60
	s_add_u32 s54, s90, s56
	s_addc_u32 s55, s91, s57
	s_add_u32 s54, s54, s53
	s_addc_u32 s55, s55, s12
	s_cmp_lg_u64 s[26:27], 0
	s_cselect_b64 s[26:27], -1, 0
	v_readlane_b32 s12, v144, s49
	s_ashr_i32 s53, s52, 31
	global_load_dwordx4 v[100:103], v128, s[58:59]
	global_load_dwordx4 v[96:99], v128, s[54:55]
	s_lshl_b64 s[52:53], s[52:53], 18
	s_lshl_b64 s[54:55], s[12:13], 10
	s_and_b64 s[50:51], s[50:51], exec
	s_cselect_b32 s12, 0, s55
	s_cselect_b32 s49, 0, s54
	s_add_u32 s50, s90, s52
	s_addc_u32 s51, s91, s53
	s_add_u32 s50, s50, s49
	s_addc_u32 s51, s51, s12
	s_cmp_lg_u64 s[24:25], 0
	s_cselect_b64 s[24:25], -1, 0
	v_readlane_b32 s12, v144, s45
	s_ashr_i32 s49, s48, 31
	s_lshl_b64 s[48:49], s[48:49], 18
	s_lshl_b64 s[52:53], s[12:13], 10
	s_and_b64 s[46:47], s[46:47], exec
	s_cselect_b32 s12, 0, s53
	s_cselect_b32 s45, 0, s52
	s_add_u32 s46, s90, s48
	s_addc_u32 s47, s91, s49
	s_add_u32 s46, s46, s45
	s_addc_u32 s47, s47, s12
	s_cmp_lg_u64 s[22:23], 0
	s_cselect_b64 s[22:23], -1, 0
	v_readlane_b32 s12, v144, s43
	s_ashr_i32 s45, s44, 31
	global_load_dwordx4 v[92:95], v128, s[50:51]
	global_load_dwordx4 v[88:91], v128, s[46:47]
	s_lshl_b64 s[44:45], s[44:45], 18
	s_lshl_b64 s[46:47], s[12:13], 10
	s_and_b64 s[20:21], s[20:21], exec
	s_cselect_b32 s12, 0, s47
	s_cselect_b32 s20, 0, s46
	s_add_u32 s21, s90, s44
	s_addc_u32 s43, s91, s45
	s_add_u32 s44, s21, s20
	s_addc_u32 s45, s43, s12
	s_cmp_lg_u64 s[18:19], 0
	s_cselect_b64 s[20:21], -1, 0
	v_readlane_b32 s12, v144, s11
	s_ashr_i32 s43, s42, 31
	s_lshl_b64 s[42:43], s[42:43], 18
	s_lshl_b64 s[46:47], s[12:13], 10
	s_and_b64 s[40:41], s[40:41], exec
	s_cselect_b32 s11, 0, s47
	s_cselect_b32 s12, 0, s46
	s_add_u32 s40, s90, s42
	s_addc_u32 s41, s91, s43
	s_add_u32 s40, s40, s12
	s_addc_u32 s41, s41, s11
	global_load_dwordx4 v[84:87], v128, s[44:45]
	global_load_dwordx4 v[80:83], v128, s[40:41]
	s_waitcnt vmcnt(36)
	v_lshlrev_b32_e32 v120, 16, v76
	v_and_b32_e32 v121, 0xffff0000, v76
	v_lshlrev_b32_e32 v122, 16, v77
	v_and_b32_e32 v123, 0xffff0000, v77
	v_lshlrev_b32_e32 v76, 16, v78
	v_and_b32_e32 v77, 0xffff0000, v78
	v_lshlrev_b32_e32 v78, 16, v79
	v_and_b32_e32 v79, 0xffff0000, v79
	v_lshlrev_b32_e32 v124, 16, v72
	v_and_b32_e32 v125, 0xffff0000, v72
	v_lshlrev_b32_e32 v126, 16, v73
	v_and_b32_e32 v127, 0xffff0000, v73
	v_lshlrev_b32_e32 v72, 16, v74
	v_and_b32_e32 v73, 0xffff0000, v74
	v_lshlrev_b32_e32 v74, 16, v75
	s_bitcmp0_b32 s7, 0
	v_and_b32_e32 v75, 0xffff0000, v75
	s_cbranch_scc1 .LBB0_1653
	s_waitcnt vmcnt(35)
	v_cvt_f32_fp8_e32 v146, v68
	v_cvt_f32_fp8_sdwa v147, v68 src0_sel:BYTE_1
	v_cvt_f32_fp8_sdwa v148, v68 src0_sel:BYTE_2
	v_cvt_f32_fp8_sdwa v149, v68 src0_sel:BYTE_3
	v_cvt_f32_fp8_e32 v150, v69
	v_cvt_f32_fp8_sdwa v151, v69 src0_sel:BYTE_1
	v_cvt_f32_fp8_sdwa v68, v69 src0_sel:BYTE_2
	v_cvt_f32_fp8_sdwa v69, v69 src0_sel:BYTE_3
	v_pk_fma_f32 v[120:121], v[146:147], s[10:11], v[120:121] op_sel_hi:[1,0,1]
	v_pk_fma_f32 v[122:123], v[148:149], s[10:11], v[122:123] op_sel_hi:[1,0,1]
	v_cvt_f32_fp8_sdwa v146, v70 src0_sel:BYTE_2
	v_pk_fma_f32 v[78:79], v[68:69], s[10:11], v[78:79] op_sel_hi:[1,0,1]
	v_cvt_f32_fp8_e32 v68, v70
	v_cvt_f32_fp8_sdwa v69, v70 src0_sel:BYTE_1
	v_cvt_f32_fp8_sdwa v147, v70 src0_sel:BYTE_3
	v_cvt_f32_fp8_e32 v148, v71
	v_cvt_f32_fp8_sdwa v149, v71 src0_sel:BYTE_1
	v_cvt_f32_fp8_sdwa v70, v71 src0_sel:BYTE_2
	v_cvt_f32_fp8_sdwa v71, v71 src0_sel:BYTE_3
	v_pk_fma_f32 v[76:77], v[150:151], s[10:11], v[76:77] op_sel_hi:[1,0,1]
	v_pk_fma_f32 v[124:125], v[68:69], s[10:11], v[124:125] op_sel_hi:[1,0,1]
	v_pk_fma_f32 v[126:127], v[146:147], s[10:11], v[126:127] op_sel_hi:[1,0,1]
	v_pk_fma_f32 v[72:73], v[148:149], s[10:11], v[72:73] op_sel_hi:[1,0,1]
	v_pk_fma_f32 v[74:75], v[70:71], s[10:11], v[74:75] op_sel_hi:[1,0,1]
	s_bitcmp0_b32 s7, 1
	s_cbranch_scc0 .LBB0_1654

; #define GAS __attribute__((address_space(1)))
; __device__ __forceinline__ bf16_t* x_row_ptr(Frame& F, int row) { return (bf16_t*)(F.ws + WS_X) + (size_t)row * D; }
; __device__ __forceinline__ void rowrq_issue(Frame& F, RowRq& R, int row, unsigned ts) {
;     R.row = row; R.ts = ts;
;     const GAS u32x4* xr = (const GAS u32x4*)x_row_ptr(F, row) + 2 * F.lane;
;     R.x[0] = xr[0]; R.x[1] = xr[1];
;     unsigned long long mask = __ballot(ts != 0xFFFFu);
;     unsigned vm = 0u;
; #pragma unroll
;     for (int k = 0; k < 8; ++k) {
;         const bool has = mask != 0ull;
;         const int e = has ? __builtin_ctzll(mask) : 0;
;         const unsigned sl = (unsigned)__builtin_amdgcn_readlane((int)ts, e);
;         mask &= mask - 1ull;
;         R.w[k] = *y_row_ptr16(F, row, has ? e : 0, has ? sl : 0u);
;         vm |= has ? (1u << k) : 0u;
;     }
;     R.vm = vm; R.rest = mask;
; }
.LBB0_1663:
	ds_write_b128 v129, v[120:123] offset:16384
	ds_write_b128 v129, v[76:79] offset:16400
	ds_write_b128 v129, v[124:127] offset:16416
	ds_write_b128 v129, v[72:75] offset:16432
	s_waitcnt lgkmcnt(0)
	s_waitcnt vmcnt(28)
	ds_read_b128 v[16:19], v140 offset:16384
	ds_read_b128 v[24:27], v141 offset:16384
	ds_read_b128 v[32:35], v142 offset:16384
	ds_read_b128 v[40:43], v143 offset:16384
	s_add_i32 s56, s87, s2
	s_ashr_i32 s57, s56, 31
	s_lshl_b64 s[6:7], s[56:57], 12
	v_lshl_add_u64 v[48:49], v[132:133], 0, s[6:7]
	s_waitcnt lgkmcnt(3)
	global_store_dwordx4 v[48:49], v[16:19], off
	s_waitcnt lgkmcnt(2)
	global_store_dwordx4 v[48:49], v[24:27], off offset:1024
	s_waitcnt lgkmcnt(1)
	global_store_dwordx4 v[48:49], v[32:35], off offset:2048
	s_waitcnt lgkmcnt(0)
	global_store_dwordx4 v[48:49], v[40:43], off offset:3072
	s_add_i32 s11, s87, 3
	s_min_i32 s12, s11, s33
	v_mov_b32_e32 v137, 0xffff
	s_and_saveexec_b64 s[6:7], s[0:1]
	v_lshl_add_u32 v16, s12, 5, v139
	ds_read_u16 v137, v16
	s_or_b64 exec, exec, s[6:7]
	s_add_i32 s6, s12, s2
	s_add_i32 s7, s6, 0xffff8000
	s_lshr_b32 s7, s7, 11
	s_waitcnt lgkmcnt(0)
	v_cmp_ne_u32_e32 vcc, s86, v137
	s_addk_i32 s7, 0x100
	s_ashr_i32 s12, s6, 11
	s_add_u32 s38, vcc_lo, -1
	s_addc_u32 s39, vcc_hi, -1
	s_and_b64 s[54:55], s[38:39], vcc
	s_add_u32 s38, s54, -1
	s_addc_u32 s39, s55, -1
	s_and_b64 s[52:53], s[38:39], s[54:55]
	s_add_u32 s38, s52, -1
	s_addc_u32 s39, s53, -1
	s_and_b64 s[50:51], s[38:39], s[52:53]
	s_add_u32 s38, s50, -1
	s_addc_u32 s39, s51, -1
	s_and_b64 s[48:49], s[38:39], s[50:51]
	s_add_u32 s38, s48, -1
	s_addc_u32 s39, s49, -1
	s_and_b64 s[46:47], s[38:39], s[48:49]
	s_add_u32 s38, s46, -1
	s_addc_u32 s39, s47, -1
	s_and_b64 s[38:39], s[38:39], s[46:47]
	s_cmp_eq_u64 s[38:39], 0
	s_cselect_b64 s[42:43], -1, 0
	s_ff1_i32_b64 s44, s[38:39]
	s_and_b64 s[40:41], s[42:43], exec
	s_cselect_b32 s59, 0, s44
	s_add_u32 s40, s38, -1
	s_addc_u32 s41, s39, -1
	s_and_b64 s[38:39], s[40:41], s[38:39]
	s_lshl_b32 s40, s59, 4
	s_add_i32 s60, s40, s12
	s_lshl_b32 s61, s59, 1
	s_cmp_eq_u64 s[38:39], 0
	s_cselect_b64 s[40:41], -1, 0
	s_ff1_i32_b64 s57, s[38:39]
	s_and_b64 s[44:45], s[40:41], exec
	s_cselect_b32 s57, 0, s57
	s_lshl_b32 s44, s57, 4
	s_lshl_b32 s45, s57, 1
	s_add_i32 s44, s44, s12
	s_add_i32 s45, s45, s7
	s_cmp_lt_i32 s6, 0x8000
	s_cselect_b32 s58, s44, s45
	s_add_i32 s61, s61, s7
	s_cmp_lt_i32 s6, 0x8000
	s_cselect_b32 s60, s60, s61
	s_cmp_eq_u64 s[46:47], 0
	s_cselect_b64 s[44:45], -1, 0
	s_ff1_i32_b64 s61, s[46:47]
	s_and_b64 s[46:47], s[44:45], exec
	s_cselect_b32 s61, 0, s61
	s_lshl_b32 s46, s61, 4
	s_lshl_b32 s47, s61, 1
	s_add_i32 s46, s46, s12
	s_add_i32 s47, s47, s7
	s_cmp_lt_i32 s6, 0x8000
	s_cselect_b32 s62, s46, s47
	s_cmp_eq_u64 s[48:49], 0
	s_cselect_b64 s[46:47], -1, 0
	s_ff1_i32_b64 s63, s[48:49]
	s_and_b64 s[48:49], s[46:47], exec
	s_cselect_b32 s63, 0, s63
	s_lshl_b32 s48, s63, 4
	s_lshl_b32 s49, s63, 1
	s_add_i32 s48, s48, s12
	s_add_i32 s49, s49, s7
	s_cmp_lt_i32 s6, 0x8000
	s_cselect_b32 s64, s48, s49
	s_cmp_eq_u64 s[50:51], 0
	s_cselect_b64 s[48:49], -1, 0
	s_ff1_i32_b64 s65, s[50:51]
	s_and_b64 s[50:51], s[48:49], exec
	s_cselect_b32 s65, 0, s65
	s_lshl_b32 s50, s65, 4
	s_lshl_b32 s51, s65, 1
	s_add_i32 s50, s50, s12
	s_add_i32 s51, s51, s7
	s_cmp_lt_i32 s6, 0x8000
	s_cselect_b32 s66, s50, s51
	s_cmp_eq_u64 s[52:53], 0
	s_cselect_b64 s[50:51], -1, 0
	s_ff1_i32_b64 s67, s[52:53]
	s_and_b64 s[52:53], s[50:51], exec
	s_cselect_b32 s67, 0, s67
	s_lshl_b32 s52, s67, 4
	s_lshl_b32 s53, s67, 1
	s_add_i32 s52, s52, s12
	s_add_i32 s53, s53, s7
	s_cmp_lt_i32 s6, 0x8000
	s_cselect_b32 s68, s52, s53
	s_cmp_eq_u64 s[54:55], 0
	s_cselect_b64 s[52:53], -1, 0
	s_ff1_i32_b64 s69, s[54:55]
	s_and_b64 s[54:55], s[52:53], exec
	s_cselect_b32 s69, 0, s69
	s_lshl_b32 s54, s69, 4
	s_lshl_b32 s55, s69, 1
	s_add_i32 s54, s54, s12
	s_add_i32 s55, s55, s7
	s_cmp_lt_i32 s6, 0x8000
	s_cselect_b32 s70, s54, s55
	s_cmp_lg_u64 vcc, 0
	s_cselect_b64 s[54:55], -1, 0
	s_ff1_i32_b64 s71, vcc
	s_and_b64 s[72:73], s[54:55], exec
	s_cselect_b32 s71, s71, 0
	s_lshl_b32 s72, s71, 4
	s_add_i32 s72, s72, s12
	s_lshl_b32 s12, s71, 1
	s_add_i32 s12, s12, s7
	s_cmp_lt_i32 s6, 0x8000
	s_cselect_b32 s72, s72, s12
	s_ashr_i32 s7, s6, 31
	s_lshl_b64 s[74:75], s[6:7], 11
	v_readlane_b32 s12, v137, s71
	s_ashr_i32 s73, s72, 31
	v_lshl_add_u64 v[16:17], v[130:131], 0, s[74:75]
	s_lshl_b64 s[72:73], s[72:73], 18
	s_lshl_b64 s[74:75], s[12:13], 10
	s_and_b64 s[76:77], s[54:55], exec
	s_cselect_b32 s7, s75, 0
	s_cselect_b32 s12, s74, 0
	s_add_u32 s71, s90, s72
	s_addc_u32 s73, s91, s73
	s_add_u32 s72, s71, s12
	s_addc_u32 s73, s73, s7
; #define GAS __attribute__((address_space(1)))
; __device__ __forceinline__ bf16_t* x_row_ptr(Frame& F, int row) { return (bf16_t*)(F.ws + WS_X) + (size_t)row * D; }
; __device__ __forceinline__ void rowrq_issue(Frame& F, RowRq& R, int row, unsigned ts) {
;     R.row = row; R.ts = ts;
;     const GAS u32x4* xr = (const GAS u32x4*)x_row_ptr(F, row) + 2 * F.lane;
;     R.x[0] = xr[0]; R.x[1] = xr[1];
;     unsigned long long mask = __ballot(ts != 0xFFFFu);
;     unsigned vm = 0u;
; #pragma unroll
;     for (int k = 0; k < 8; ++k) {
;         const bool has = mask != 0ull;
;         const int e = has ? __builtin_ctzll(mask) : 0;
;         const unsigned sl = (unsigned)__builtin_amdgcn_readlane((int)ts, e);
;         mask &= mask - 1ull;
;         R.w[k] = *y_row_ptr16(F, row, has ? e : 0, has ? sl : 0u);
;         vm |= has ? (1u << k) : 0u;
;     }
;     R.vm = vm; R.rest = mask;
; }
; __device__ __forceinline__ void rowrq_consume(Frame& F, const RowRq& R, f32x4 (&v)[4]) {
; #pragma unroll
;     for (int h = 0; h < 2; ++h) { const u32x4 x = R.x[h]; v[2 * h] = (f32x4){bf_lo(x.x), bf_hi(x.x), bf_lo(x.y), bf_hi(x.y)}; v[2 * h + 1] = (f32x4){bf_lo(x.z), bf_hi(x.z), bf_lo(x.w), bf_hi(x.w)}; }
; #pragma unroll
;     for (int k = 0; k < 8; ++k)
;         if ((R.vm >> k) & 1u) {
; #pragma unroll
;             for (int q = 0; q < 4; ++q) y_add4(v[q], R.w[k][q]); }
	v_readlane_b32 s12, v137, s69
	s_ashr_i32 s71, s70, 31
	s_lshl_b64 s[70:71], s[70:71], 18
	s_lshl_b64 s[74:75], s[12:13], 10
	s_and_b64 s[76:77], s[52:53], exec
	s_cselect_b32 s7, 0, s75
	s_cselect_b32 s12, 0, s74
	s_add_u32 s69, s90, s70
	s_addc_u32 s71, s91, s71
	s_add_u32 s70, s69, s12
	s_addc_u32 s71, s71, s7
	v_readlane_b32 s12, v137, s67
	s_ashr_i32 s69, s68, 31
	global_load_dwordx4 v[72:75], v[16:17], off offset:16 nt
	global_load_dwordx4 v[76:79], v[16:17], off nt
	global_load_dwordx4 v[68:71], v128, s[72:73]
	global_load_dwordx4 v[64:67], v128, s[70:71]
	s_lshl_b64 s[68:69], s[68:69], 18
	s_lshl_b64 s[70:71], s[12:13], 10
	s_and_b64 s[72:73], s[50:51], exec
	s_cselect_b32 s7, 0, s71
	s_cselect_b32 s12, 0, s70
	s_add_u32 s67, s90, s68
	s_addc_u32 s69, s91, s69
	s_add_u32 s68, s67, s12
	s_addc_u32 s69, s69, s7
	v_readlane_b32 s12, v137, s65
	s_ashr_i32 s67, s66, 31
	s_lshl_b64 s[66:67], s[66:67], 18
	s_lshl_b64 s[70:71], s[12:13], 10
	s_and_b64 s[72:73], s[48:49], exec
	s_cselect_b32 s7, 0, s71
	s_cselect_b32 s12, 0, s70
	s_add_u32 s65, s90, s66
	s_addc_u32 s67, s91, s67
	s_add_u32 s66, s65, s12
	s_addc_u32 s67, s67, s7
	v_readlane_b32 s12, v137, s63
	s_ashr_i32 s65, s64, 31
	global_load_dwordx4 v[60:63], v128, s[68:69]
	global_load_dwordx4 v[48:51], v128, s[66:67]
	s_lshl_b64 s[64:65], s[64:65], 18
	s_lshl_b64 s[66:67], s[12:13], 10
	s_and_b64 s[68:69], s[46:47], exec
	s_cselect_b32 s7, 0, s67
	s_cselect_b32 s12, 0, s66
	s_add_u32 s63, s90, s64
	s_addc_u32 s65, s91, s65
	s_add_u32 s64, s63, s12
	s_addc_u32 s65, s65, s7
	v_readlane_b32 s12, v137, s61
	s_ashr_i32 s63, s62, 31
	s_lshl_b64 s[62:63], s[62:63], 18
	s_lshl_b64 s[66:67], s[12:13], 10
	s_and_b64 s[68:69], s[44:45], exec
	s_cselect_b32 s7, 0, s67
	s_cselect_b32 s12, 0, s66
	s_add_u32 s61, s90, s62
	s_addc_u32 s63, s91, s63
	s_add_u32 s62, s61, s12
	s_addc_u32 s63, s63, s7
	v_readlane_b32 s12, v137, s59
	s_ashr_i32 s61, s60, 31
	global_load_dwordx4 v[40:43], v128, s[64:65]
	global_load_dwordx4 v[32:35], v128, s[62:63]
	s_lshl_b64 s[60:61], s[60:61], 18
	s_lshl_b64 s[62:63], s[12:13], 10
	s_and_b64 s[64:65], s[42:43], exec
	s_cselect_b32 s7, 0, s63
	s_cselect_b32 s12, 0, s62
	s_add_u32 s59, s90, s60
	s_addc_u32 s61, s91, s61
	s_add_u32 s60, s59, s12
	s_addc_u32 s61, s61, s7
	v_readlane_b32 s12, v137, s57
	s_ashr_i32 s59, s58, 31
	s_lshl_b64 s[58:59], s[58:59], 18
	s_lshl_b64 s[62:63], s[12:13], 10
	s_and_b64 s[64:65], s[40:41], exec
	s_cselect_b32 s7, 0, s63
	s_cselect_b32 s12, 0, s62
	s_add_u32 s57, s90, s58
	s_addc_u32 s59, s91, s59
	s_add_u32 s58, s57, s12
	s_addc_u32 s59, s59, s7
	global_load_dwordx4 v[24:27], v128, s[60:61]
	global_load_dwordx4 v[16:19], v128, s[58:59]
	s_waitcnt vmcnt(32)
	v_lshlrev_b32_e32 v120, 16, v56
	v_and_b32_e32 v121, 0xffff0000, v56
	v_lshlrev_b32_e32 v122, 16, v57
	v_and_b32_e32 v123, 0xffff0000, v57
	v_lshlrev_b32_e32 v56, 16, v58
	v_and_b32_e32 v57, 0xffff0000, v58
	v_lshlrev_b32_e32 v58, 16, v59
	v_and_b32_e32 v59, 0xffff0000, v59
	v_lshlrev_b32_e32 v124, 16, v52
	v_and_b32_e32 v125, 0xffff0000, v52
	v_lshlrev_b32_e32 v126, 16, v53
	v_and_b32_e32 v127, 0xffff0000, v53
	v_lshlrev_b32_e32 v52, 16, v54
	v_and_b32_e32 v53, 0xffff0000, v54
	v_lshlrev_b32_e32 v54, 16, v55
	s_bitcmp0_b32 s5, 0
	v_and_b32_e32 v55, 0xffff0000, v55
	s_cbranch_scc1 .LBB0_1674
	s_waitcnt vmcnt(31)
	v_cvt_f32_fp8_e32 v146, v44
	v_cvt_f32_fp8_sdwa v147, v44 src0_sel:BYTE_1
	v_cvt_f32_fp8_sdwa v148, v44 src0_sel:BYTE_2
	v_cvt_f32_fp8_sdwa v149, v44 src0_sel:BYTE_3
	v_cvt_f32_fp8_e32 v150, v45
	v_cvt_f32_fp8_sdwa v151, v45 src0_sel:BYTE_1
	v_cvt_f32_fp8_sdwa v44, v45 src0_sel:BYTE_2
	v_cvt_f32_fp8_sdwa v45, v45 src0_sel:BYTE_3
	v_pk_fma_f32 v[120:121], v[146:147], s[10:11], v[120:121] op_sel_hi:[1,0,1]
	v_pk_fma_f32 v[122:123], v[148:149], s[10:11], v[122:123] op_sel_hi:[1,0,1]
	v_cvt_f32_fp8_sdwa v146, v46 src0_sel:BYTE_2
	v_pk_fma_f32 v[58:59], v[44:45], s[10:11], v[58:59] op_sel_hi:[1,0,1]
	v_cvt_f32_fp8_e32 v44, v46
	v_cvt_f32_fp8_sdwa v45, v46 src0_sel:BYTE_1
	v_cvt_f32_fp8_sdwa v147, v46 src0_sel:BYTE_3
	v_cvt_f32_fp8_e32 v148, v47
	v_cvt_f32_fp8_sdwa v149, v47 src0_sel:BYTE_1
	v_cvt_f32_fp8_sdwa v46, v47 src0_sel:BYTE_2
	v_cvt_f32_fp8_sdwa v47, v47 src0_sel:BYTE_3
	v_pk_fma_f32 v[56:57], v[150:151], s[10:11], v[56:57] op_sel_hi:[1,0,1]
	v_pk_fma_f32 v[124:125], v[44:45], s[10:11], v[124:125] op_sel_hi:[1,0,1]
	v_pk_fma_f32 v[126:127], v[146:147], s[10:11], v[126:127] op_sel_hi:[1,0,1]
	v_pk_fma_f32 v[52:53], v[148:149], s[10:11], v[52:53] op_sel_hi:[1,0,1]
	v_pk_fma_f32 v[54:55], v[46:47], s[10:11], v[54:55] op_sel_hi:[1,0,1]
	s_bitcmp0_b32 s5, 1
	s_cbranch_scc0 .LBB0_1675

; #define GAS __attribute__((address_space(1)))
; __device__ __forceinline__ bf16_t* x_row_ptr(Frame& F, int row) { return (bf16_t*)(F.ws + WS_X) + (size_t)row * D; }
; __device__ __forceinline__ void rowrq_issue(Frame& F, RowRq& R, int row, unsigned ts) {
;     R.row = row; R.ts = ts;
;     const GAS u32x4* xr = (const GAS u32x4*)x_row_ptr(F, row) + 2 * F.lane;
;     R.x[0] = xr[0]; R.x[1] = xr[1];
;     unsigned long long mask = __ballot(ts != 0xFFFFu);
;     unsigned vm = 0u;
; #pragma unroll
;     for (int k = 0; k < 8; ++k) {
;         const bool has = mask != 0ull;
;         const int e = has ? __builtin_ctzll(mask) : 0;
;         const unsigned sl = (unsigned)__builtin_amdgcn_readlane((int)ts, e);
;         mask &= mask - 1ull;
;         R.w[k] = *y_row_ptr16(F, row, has ? e : 0, has ? sl : 0u);
;         vm |= has ? (1u << k) : 0u;
;     }
;     R.vm = vm; R.rest = mask;
; }
.LBB0_1684:
	ds_write_b128 v129, v[120:123] offset:16384
	ds_write_b128 v129, v[56:59] offset:16400
	ds_write_b128 v129, v[124:127] offset:16416
	ds_write_b128 v129, v[52:55] offset:16432
	s_waitcnt lgkmcnt(0)
	s_waitcnt vmcnt(24)
	ds_read_b128 v[0:3], v140 offset:16384
	ds_read_b128 v[4:7], v141 offset:16384
	ds_read_b128 v[8:11], v142 offset:16384
	ds_read_b128 v[12:15], v143 offset:16384
	s_add_i32 s4, s56, 1
	s_ashr_i32 s5, s4, 31
	s_lshl_b64 s[4:5], s[4:5], 12
	v_lshl_add_u64 v[20:21], v[132:133], 0, s[4:5]
	s_waitcnt lgkmcnt(3)
	global_store_dwordx4 v[20:21], v[0:3], off
	s_waitcnt lgkmcnt(2)
	global_store_dwordx4 v[20:21], v[4:7], off offset:1024
	s_waitcnt lgkmcnt(1)
	global_store_dwordx4 v[20:21], v[8:11], off offset:2048
	s_waitcnt lgkmcnt(0)
	global_store_dwordx4 v[20:21], v[12:15], off offset:3072
	s_add_i32 s4, s87, 4
	s_min_i32 s7, s4, s33
	v_mov_b32_e32 v135, 0xffff
	s_and_saveexec_b64 s[4:5], s[0:1]
	v_lshl_add_u32 v0, s7, 5, v139
	ds_read_u16 v135, v0
	s_or_b64 exec, exec, s[4:5]
	s_add_i32 s4, s7, s2
	s_add_i32 s5, s4, 0xffff8000
	s_lshr_b32 s5, s5, 11
	s_waitcnt lgkmcnt(0)
	v_cmp_ne_u32_e32 vcc, s86, v135
	s_addk_i32 s5, 0x100
	s_ashr_i32 s12, s4, 11
	s_add_u32 s8, vcc_lo, -1
	s_addc_u32 s9, vcc_hi, -1
	s_and_b64 s[70:71], s[8:9], vcc
	s_add_u32 s8, s70, -1
	s_addc_u32 s9, s71, -1
	s_and_b64 s[68:69], s[8:9], s[70:71]
	s_add_u32 s8, s68, -1
	s_addc_u32 s9, s69, -1
	s_and_b64 s[66:67], s[8:9], s[68:69]
	s_add_u32 s8, s66, -1
	s_addc_u32 s9, s67, -1
	s_and_b64 s[64:65], s[8:9], s[66:67]
	s_add_u32 s8, s64, -1
	s_addc_u32 s9, s65, -1
	s_and_b64 s[62:63], s[8:9], s[64:65]
	s_add_u32 s8, s62, -1
	s_addc_u32 s9, s63, -1
	s_and_b64 s[8:9], s[8:9], s[62:63]
	s_cmp_eq_u64 s[8:9], 0
	s_cselect_b64 s[58:59], -1, 0
	s_ff1_i32_b64 s7, s[8:9]
	s_and_b64 s[56:57], s[58:59], exec
	s_cselect_b32 s73, 0, s7
	s_add_u32 s56, s8, -1
	s_addc_u32 s57, s9, -1
	s_lshl_b32 s7, s73, 4
	s_and_b64 s[8:9], s[56:57], s[8:9]
	s_add_i32 s74, s7, s12
	s_lshl_b32 s75, s73, 1
	s_cmp_eq_u64 s[8:9], 0
	s_cselect_b64 s[56:57], -1, 0
	s_ff1_i32_b64 s7, s[8:9]
	s_and_b64 s[60:61], s[56:57], exec
	s_cselect_b32 s7, 0, s7
	s_lshl_b32 s60, s7, 4
	s_lshl_b32 s61, s7, 1
	s_add_i32 s60, s60, s12
	s_add_i32 s61, s61, s5
	s_cmp_lt_i32 s4, 0x8000
	s_cselect_b32 s72, s60, s61
	s_add_i32 s75, s75, s5
	s_cmp_lt_i32 s4, 0x8000
	s_cselect_b32 s74, s74, s75
	s_cmp_eq_u64 s[62:63], 0
	s_cselect_b64 s[60:61], -1, 0
	s_ff1_i32_b64 s75, s[62:63]
	s_and_b64 s[62:63], s[60:61], exec
	s_cselect_b32 s75, 0, s75
	s_lshl_b32 s62, s75, 4
	s_lshl_b32 s63, s75, 1
	s_add_i32 s62, s62, s12
	s_add_i32 s63, s63, s5
	s_cmp_lt_i32 s4, 0x8000
	s_cselect_b32 s76, s62, s63
	s_cmp_eq_u64 s[64:65], 0
	s_cselect_b64 s[62:63], -1, 0
	s_ff1_i32_b64 s77, s[64:65]
	s_and_b64 s[64:65], s[62:63], exec
	s_cselect_b32 s77, 0, s77
	s_lshl_b32 s64, s77, 4
	s_lshl_b32 s65, s77, 1
	s_add_i32 s64, s64, s12
	s_add_i32 s65, s65, s5
	s_cmp_lt_i32 s4, 0x8000
	s_cselect_b32 s78, s64, s65
	s_cmp_eq_u64 s[66:67], 0
	s_cselect_b64 s[64:65], -1, 0
	s_ff1_i32_b64 s79, s[66:67]
	s_and_b64 s[66:67], s[64:65], exec
	s_cselect_b32 s79, 0, s79
	s_lshl_b32 s66, s79, 4
	s_lshl_b32 s67, s79, 1
	s_add_i32 s66, s66, s12
	s_add_i32 s67, s67, s5
	s_cmp_lt_i32 s4, 0x8000
	s_cselect_b32 s82, s66, s67
	s_cmp_eq_u64 s[68:69], 0
	s_cselect_b64 s[66:67], -1, 0
	s_ff1_i32_b64 s83, s[68:69]
	s_and_b64 s[68:69], s[66:67], exec
	s_cselect_b32 s83, 0, s83
	s_lshl_b32 s68, s83, 4
	s_lshl_b32 s69, s83, 1
	s_add_i32 s68, s68, s12
	s_add_i32 s69, s69, s5
	s_cmp_lt_i32 s4, 0x8000
	s_cselect_b32 s92, s68, s69
	s_cmp_eq_u64 s[70:71], 0
	s_cselect_b64 s[68:69], -1, 0
	s_ff1_i32_b64 s84, s[70:71]
	s_and_b64 s[70:71], s[68:69], exec
	s_cselect_b32 s93, 0, s84
	s_lshl_b32 s70, s93, 4
	s_lshl_b32 s71, s93, 1
	s_add_i32 s70, s70, s12
	s_add_i32 s71, s71, s5
	s_cmp_lt_i32 s4, 0x8000
	s_cselect_b32 s94, s70, s71
	s_cmp_lg_u64 vcc, 0
	s_cselect_b64 s[70:71], -1, 0
	s_ff1_i32_b64 s84, vcc
	s_and_b64 s[96:97], s[70:71], exec
	s_cselect_b32 s84, s84, 0
	s_lshl_b32 s85, s84, 4
	s_add_i32 s85, s85, s12
	s_lshl_b32 s12, s84, 1
	s_add_i32 s12, s12, s5
	s_cmp_lt_i32 s4, 0x8000
	s_cselect_b32 s96, s85, s12
	s_ashr_i32 s5, s4, 31
	s_lshl_b64 vcc, s[4:5], 11
	v_readlane_b32 s12, v135, s84
	s_ashr_i32 s97, s96, 31
	v_lshl_add_u64 v[0:1], v[130:131], 0, vcc
	s_lshl_b64 s[96:97], s[96:97], 18
	s_lshl_b64 vcc, s[12:13], 10
	s_and_b64 s[84:85], s[70:71], exec
	s_cselect_b32 s5, vcc_hi, 0
	s_cselect_b32 s12, vcc_lo, 0
	s_add_u32 s84, s90, s96
	s_addc_u32 s85, s91, s97
	s_add_u32 s84, s84, s12
	s_addc_u32 s85, s85, s5
	v_readlane_b32 s12, v135, s93
	s_ashr_i32 s95, s94, 31
; #define GAS __attribute__((address_space(1)))
; __device__ __forceinline__ bf16_t* x_row_ptr(Frame& F, int row) { return (bf16_t*)(F.ws + WS_X) + (size_t)row * D; }
; __device__ __forceinline__ void rowrq_issue(Frame& F, RowRq& R, int row, unsigned ts) {
;     R.row = row; R.ts = ts;
;     const GAS u32x4* xr = (const GAS u32x4*)x_row_ptr(F, row) + 2 * F.lane;
;     R.x[0] = xr[0]; R.x[1] = xr[1];
;     unsigned long long mask = __ballot(ts != 0xFFFFu);
;     unsigned vm = 0u;
; #pragma unroll
;     for (int k = 0; k < 8; ++k) {
;         const bool has = mask != 0ull;
;         const int e = has ? __builtin_ctzll(mask) : 0;
;         const unsigned sl = (unsigned)__builtin_amdgcn_readlane((int)ts, e);
;         mask &= mask - 1ull;
;         R.w[k] = *y_row_ptr16(F, row, has ? e : 0, has ? sl : 0u);
;         vm |= has ? (1u << k) : 0u;
;     }
;     R.vm = vm; R.rest = mask;
; }
; __device__ __forceinline__ void rowrq_consume(Frame& F, const RowRq& R, f32x4 (&v)[4]) {
; #pragma unroll
;     for (int h = 0; h < 2; ++h) { const u32x4 x = R.x[h]; v[2 * h] = (f32x4){bf_lo(x.x), bf_hi(x.x), bf_lo(x.y), bf_hi(x.y)}; v[2 * h + 1] = (f32x4){bf_lo(x.z), bf_hi(x.z), bf_lo(x.w), bf_hi(x.w)}; }
; #pragma unroll
;     for (int k = 0; k < 8; ++k)
;         if ((R.vm >> k) & 1u) {
; #pragma unroll
;             for (int q = 0; q < 4; ++q) y_add4(v[q], R.w[k][q]); }
	s_lshl_b64 s[94:95], s[94:95], 18
	s_lshl_b64 s[96:97], s[12:13], 10
	s_and_b64 vcc, s[68:69], exec
	s_cselect_b32 s5, 0, s97
	s_cselect_b32 s12, 0, s96
	s_add_u32 s93, s90, s94
	s_addc_u32 s95, s91, s95
	s_add_u32 s94, s93, s12
	s_addc_u32 s95, s95, s5
	v_readlane_b32 s12, v135, s83
	s_ashr_i32 s93, s92, 31
	global_load_dwordx4 v[52:55], v[0:1], off offset:16 nt
	global_load_dwordx4 v[56:59], v[0:1], off nt
	global_load_dwordx4 v[44:47], v128, s[84:85]
	global_load_dwordx4 v[36:39], v128, s[94:95]
	s_lshl_b64 s[84:85], s[92:93], 18
	s_lshl_b64 s[92:93], s[12:13], 10
	s_and_b64 s[94:95], s[66:67], exec
	s_cselect_b32 s5, 0, s93
	s_cselect_b32 s12, 0, s92
	s_add_u32 s83, s90, s84
	s_addc_u32 s85, s91, s85
	s_add_u32 s84, s83, s12
	s_addc_u32 s85, s85, s5
	v_readlane_b32 s12, v135, s79
	s_ashr_i32 s83, s82, 31
	s_lshl_b64 s[82:83], s[82:83], 18
	s_lshl_b64 s[92:93], s[12:13], 10
	s_and_b64 s[94:95], s[64:65], exec
	s_cselect_b32 s5, 0, s93
	s_cselect_b32 s12, 0, s92
	s_add_u32 s79, s90, s82
	s_addc_u32 s83, s91, s83
	s_add_u32 s82, s79, s12
	s_addc_u32 s83, s83, s5
	v_readlane_b32 s12, v135, s77
	s_ashr_i32 s79, s78, 31
	global_load_dwordx4 v[28:31], v128, s[84:85]
	global_load_dwordx4 v[20:23], v128, s[82:83]
	s_lshl_b64 s[78:79], s[78:79], 18
	s_lshl_b64 s[82:83], s[12:13], 10
	s_and_b64 s[84:85], s[62:63], exec
	s_cselect_b32 s5, 0, s83
	s_cselect_b32 s12, 0, s82
	s_add_u32 s77, s90, s78
	s_addc_u32 s79, s91, s79
	s_add_u32 s78, s77, s12
	s_addc_u32 s79, s79, s5
	v_readlane_b32 s12, v135, s75
	s_ashr_i32 s77, s76, 31
	s_lshl_b64 s[76:77], s[76:77], 18
	s_lshl_b64 s[82:83], s[12:13], 10
	s_and_b64 s[84:85], s[60:61], exec
	s_cselect_b32 s5, 0, s83
	s_cselect_b32 s12, 0, s82
	s_add_u32 s75, s90, s76
	s_addc_u32 s77, s91, s77
	s_add_u32 s76, s75, s12
	s_addc_u32 s77, s77, s5
	v_readlane_b32 s12, v135, s73
	s_ashr_i32 s75, s74, 31
	global_load_dwordx4 v[12:15], v128, s[78:79]
	global_load_dwordx4 v[8:11], v128, s[76:77]
	s_lshl_b64 s[74:75], s[74:75], 18
	s_lshl_b64 s[76:77], s[12:13], 10
	s_and_b64 s[78:79], s[58:59], exec
	s_cselect_b32 s5, 0, s77
	s_cselect_b32 s12, 0, s76
	s_add_u32 s73, s90, s74
	s_addc_u32 s75, s91, s75
	s_add_u32 s74, s73, s12
	s_addc_u32 s75, s75, s5
	v_readlane_b32 s12, v135, s7
	s_ashr_i32 s73, s72, 31
	s_lshl_b64 s[72:73], s[72:73], 18
	s_lshl_b64 s[76:77], s[12:13], 10
	s_and_b64 s[78:79], s[56:57], exec
	s_cselect_b32 s5, 0, s77
	s_cselect_b32 s7, 0, s76
	s_add_u32 s12, s90, s72
	s_addc_u32 s73, s91, s73
	s_add_u32 s72, s12, s7
	s_addc_u32 s73, s73, s5
	global_load_dwordx4 v[4:7], v128, s[74:75]
	global_load_dwordx4 v[0:3], v128, s[72:73]
	s_waitcnt vmcnt(36)
	v_lshlrev_b32_e32 v120, 16, v116
	v_and_b32_e32 v121, 0xffff0000, v116
	v_lshlrev_b32_e32 v122, 16, v117
	v_and_b32_e32 v123, 0xffff0000, v117
	v_lshlrev_b32_e32 v116, 16, v118
	v_and_b32_e32 v117, 0xffff0000, v118
	v_lshlrev_b32_e32 v118, 16, v119
	v_and_b32_e32 v119, 0xffff0000, v119
	v_lshlrev_b32_e32 v124, 16, v112
	v_and_b32_e32 v125, 0xffff0000, v112
	v_lshlrev_b32_e32 v126, 16, v113
	v_and_b32_e32 v127, 0xffff0000, v113
	v_lshlrev_b32_e32 v112, 16, v114
	v_and_b32_e32 v113, 0xffff0000, v114
	v_lshlrev_b32_e32 v114, 16, v115
	s_andn2_b64 vcc, exec, s[36:37]
	v_and_b32_e32 v115, 0xffff0000, v115
	s_cbranch_vccnz .LBB0_1694
	s_waitcnt vmcnt(35)
	v_cvt_f32_fp8_e32 v146, v108
	v_cvt_f32_fp8_sdwa v147, v108 src0_sel:BYTE_1
	v_cvt_f32_fp8_sdwa v148, v108 src0_sel:BYTE_2
	v_cvt_f32_fp8_sdwa v149, v108 src0_sel:BYTE_3
	v_cvt_f32_fp8_e32 v150, v109
	v_cvt_f32_fp8_sdwa v151, v109 src0_sel:BYTE_1
	v_cvt_f32_fp8_sdwa v108, v109 src0_sel:BYTE_2
	v_cvt_f32_fp8_sdwa v109, v109 src0_sel:BYTE_3
	v_pk_fma_f32 v[120:121], v[146:147], s[10:11], v[120:121] op_sel_hi:[1,0,1]
	v_pk_fma_f32 v[122:123], v[148:149], s[10:11], v[122:123] op_sel_hi:[1,0,1]
	v_cvt_f32_fp8_sdwa v146, v110 src0_sel:BYTE_2
	v_pk_fma_f32 v[118:119], v[108:109], s[10:11], v[118:119] op_sel_hi:[1,0,1]
	v_cvt_f32_fp8_e32 v108, v110
	v_cvt_f32_fp8_sdwa v109, v110 src0_sel:BYTE_1
	v_cvt_f32_fp8_sdwa v147, v110 src0_sel:BYTE_3
	v_cvt_f32_fp8_e32 v148, v111
	v_cvt_f32_fp8_sdwa v149, v111 src0_sel:BYTE_1
	v_cvt_f32_fp8_sdwa v110, v111 src0_sel:BYTE_2
	v_cvt_f32_fp8_sdwa v111, v111 src0_sel:BYTE_3
	v_pk_fma_f32 v[116:117], v[150:151], s[10:11], v[116:117] op_sel_hi:[1,0,1]
	v_pk_fma_f32 v[124:125], v[108:109], s[10:11], v[124:125] op_sel_hi:[1,0,1]
	v_pk_fma_f32 v[126:127], v[146:147], s[10:11], v[126:127] op_sel_hi:[1,0,1]
	v_pk_fma_f32 v[112:113], v[148:149], s[10:11], v[112:113] op_sel_hi:[1,0,1]
	v_pk_fma_f32 v[114:115], v[110:111], s[10:11], v[114:115] op_sel_hi:[1,0,1]
	s_andn2_b64 vcc, exec, s[34:35]
	s_cbranch_vccz .LBB0_1695
